# baseline (speedup 1.0000x reference)
.LE_join19:
	s_waitcnt lgkmcnt(2)
	v_mfma_f32_32x32x16_f16 v[0:15], a[168:171], v[176:179], v[0:15]
	ds_read_b128 v[176:179], v193 offset:28672
	v_mfma_f32_32x32x16_f16 v[16:31], a[168:171], v[180:183], v[16:31]
	ds_read_b128 v[180:183], v193 offset:29696
	v_mfma_f32_32x32x16_f16 v[0:15], a[172:175], v[184:187], v[0:15]
	ds_read_b128 v[184:187], v193 offset:30720
	v_mfma_f32_32x32x16_f16 v[16:31], a[172:175], v[188:191], v[16:31]
	ds_read_b128 v[188:191], v193 offset:31744
	global_load_lds_dwordx4 v192, s[44:45] offset:2048 sc1
	s_waitcnt vmcnt(8)
	s_barrier
	v_mfma_f32_32x32x16_f16 v[0:15], a[176:179], v[160:163], v[0:15]
	ds_read_b128 v[160:163], v193 offset:32768
	v_mfma_f32_32x32x16_f16 v[16:31], a[176:179], v[164:167], v[16:31]
	ds_read_b128 v[164:167], v193 offset:33792
	s_waitcnt lgkmcnt(2)
	v_mfma_f32_32x32x16_f16 v[0:15], a[180:183], v[168:171], v[0:15]
	ds_read_b128 v[168:171], v193 offset:34816
	v_mfma_f32_32x32x16_f16 v[16:31], a[180:183], v[172:175], v[16:31]
	ds_read_b128 v[172:175], v193 offset:35840
	global_load_lds_dwordx4 v192, s[44:45] offset:3072 sc1
	v_mfma_f32_32x32x16_f16 v[0:15], a[184:187], v[176:179], v[0:15]
	ds_read_b128 v[176:179], v193 offset:36864
	v_mfma_f32_32x32x16_f16 v[16:31], a[184:187], v[180:183], v[16:31]
	ds_read_b128 v[180:183], v193 offset:37888
	v_mfma_f32_32x32x16_f16 v[0:15], a[188:191], v[184:187], v[0:15]
	ds_read_b128 v[184:187], v193 offset:38912
	v_mfma_f32_32x32x16_f16 v[16:31], a[188:191], v[188:191], v[16:31]
	ds_read_b128 v[188:191], v193 offset:39936
	s_mov_b32 m0, s54
	s_add_u32 s44, s34, 0x8000
	s_addc_u32 s45, s35, 0
	global_load_lds_dwordx4 v192, s[44:45] sc1
	s_waitcnt lgkmcnt(2)
	v_mfma_f32_32x32x16_f16 v[0:15], a[192:195], v[160:163], v[0:15]
	ds_read_b128 v[160:163], v193 offset:40960
	v_mfma_f32_32x32x16_f16 v[16:31], a[192:195], v[164:167], v[16:31]
	ds_read_b128 v[164:167], v193 offset:41984
	v_mfma_f32_32x32x16_f16 v[0:15], a[196:199], v[168:171], v[0:15]
	ds_read_b128 v[168:171], v193 offset:43008
	v_mfma_f32_32x32x16_f16 v[16:31], a[196:199], v[172:175], v[16:31]
	ds_read_b128 v[172:175], v193 offset:44032
	global_load_lds_dwordx4 v192, s[44:45] offset:1024 sc1
	v_mfma_f32_32x32x16_f16 v[0:15], a[200:203], v[176:179], v[0:15]
	ds_read_b128 v[176:179], v193 offset:45056
	v_mfma_f32_32x32x16_f16 v[16:31], a[200:203], v[180:183], v[16:31]
	ds_read_b128 v[180:183], v193 offset:46080
	s_waitcnt lgkmcnt(2)
	v_mfma_f32_32x32x16_f16 v[0:15], a[204:207], v[184:187], v[0:15]
	ds_read_b128 v[184:187], v193 offset:47104
	v_mfma_f32_32x32x16_f16 v[16:31], a[204:207], v[188:191], v[16:31]
	ds_read_b128 v[188:191], v193 offset:48128
	global_load_lds_dwordx4 v192, s[44:45] offset:2048 sc1
	v_mfma_f32_32x32x16_f16 v[0:15], a[208:211], v[160:163], v[0:15]
	ds_read_b128 v[160:163], v193 offset:49152
	s_waitcnt vmcnt(5)
	s_barrier
	v_mov_b32_e32 v199, 4
	s_cmp_eq_u32 s31, 0
	s_cbranch_scc1 .LE_slow20
	global_store_dword v197, v199, s[40:41]
.LE_join21:
	v_mfma_f32_32x32x16_f16 v[16:31], a[208:211], v[164:167], v[16:31]
	ds_read_b128 v[164:167], v193 offset:50176
	v_mfma_f32_32x32x16_f16 v[0:15], a[212:215], v[168:171], v[0:15]
	ds_read_b128 v[168:171], v193 offset:51200
	v_mfma_f32_32x32x16_f16 v[16:31], a[212:215], v[172:175], v[16:31]
	ds_read_b128 v[172:175], v193 offset:52224
	global_load_lds_dwordx4 v192, s[44:45] offset:3072 sc1
	s_waitcnt lgkmcnt(2)
	v_mfma_f32_32x32x16_f16 v[0:15], a[216:219], v[176:179], v[0:15]
	ds_read_b128 v[176:179], v193 offset:53248
	s_and_b32 s64, s33, 1
	s_lshl_b32 s64, s64, 22
	s_add_u32 s64, s64, s50
	s_add_u32 s36, s6, s64
	s_addc_u32 s37, s7, 0
	s_lshl_b32 s64, s33, 3
	s_add_u32 s64, s64, s29
	s_lshl_b32 s64, s64, 5
	s_add_u32 s64, s64, s30
	s_lshl_b32 s64, s64, 2
	s_add_u32 s40, s8, s64
	s_addc_u32 s41, s9, 0
	s_lshl_b32 s64, s33, 11
	s_lshl_b32 s65, s29, 8
	s_add_u32 s64, s64, s65
	s_add_u32 s64, s64, 192
	s_lshl_b32 s64, s64, 3
	s_add_u32 s42, s12, s64
	s_addc_u32 s43, s13, 0
	v_mfma_f32_32x32x16_f16 v[16:31], a[216:219], v[180:183], v[16:31]
	ds_read_b128 v[180:183], v193 offset:54272
	v_mfma_f32_32x32x16_f16 v[0:15], a[220:223], v[184:187], v[0:15]
	ds_read_b128 v[184:187], v193 offset:55296
	v_mfma_f32_32x32x16_f16 v[16:31], a[220:223], v[188:191], v[16:31]
	ds_read_b128 v[188:191], v193 offset:56320
	s_mov_b32 m0, s55
	s_add_u32 s44, s34, 0x9000
	s_addc_u32 s45, s35, 0
	global_load_lds_dwordx4 v192, s[44:45] sc1
	v_mfma_f32_32x32x16_f16 v[0:15], a[224:227], v[160:163], v[0:15]
	ds_read_b128 v[160:163], v193 offset:57344
	v_mfma_f32_32x32x16_f16 v[16:31], a[224:227], v[164:167], v[16:31]
	ds_read_b128 v[164:167], v193 offset:58368
	s_waitcnt lgkmcnt(2)
	v_mfma_f32_32x32x16_f16 v[0:15], a[228:231], v[168:171], v[0:15]
	ds_read_b128 v[168:171], v193 offset:59392
	v_mfma_f32_32x32x16_f16 v[16:31], a[228:231], v[172:175], v[16:31]
	ds_read_b128 v[172:175], v193 offset:60416
	global_load_lds_dwordx4 v192, s[44:45] offset:1024 sc1
	v_mfma_f32_32x32x16_f16 v[0:15], a[232:235], v[176:179], v[0:15]
	ds_read_b128 v[176:179], v193 offset:61440
	v_mfma_f32_32x32x16_f16 v[16:31], a[232:235], v[180:183], v[16:31]
	ds_read_b128 v[180:183], v193 offset:62464
	v_mfma_f32_32x32x16_f16 v[0:15], a[236:239], v[184:187], v[0:15]
	ds_read_b128 v[184:187], v193 offset:63488
	v_mfma_f32_32x32x16_f16 v[16:31], a[236:239], v[188:191], v[16:31]
	ds_read_b128 v[188:191], v193 offset:64512
	global_load_lds_dwordx4 v192, s[44:45] offset:2048 sc1
	s_waitcnt vmcnt(8)
	s_barrier
	s_waitcnt lgkmcnt(2)
	v_mfma_f32_32x32x16_f16 v[0:15], a[240:243], v[160:163], v[0:15]
	ds_read_b128 v[160:163], v192 offset:0
	v_mfma_f32_32x32x16_f16 v[16:31], a[240:243], v[164:167], v[16:31]
	ds_read_b128 v[164:167], v192 offset:1024
	v_mfma_f32_32x32x16_f16 v[0:15], a[244:247], v[168:171], v[0:15]
	ds_read_b128 v[168:171], v192 offset:2048
	v_mfma_f32_32x32x16_f16 v[16:31], a[244:247], v[172:175], v[16:31]
	ds_read_b128 v[172:175], v192 offset:3072
	global_load_lds_dwordx4 v192, s[44:45] offset:3072 sc1
	v_mfma_f32_32x32x16_f16 v[0:15], a[248:251], v[176:179], v[0:15]
	ds_read_b128 v[176:179], v192 offset:4096
	v_mfma_f32_32x32x16_f16 v[16:31], a[248:251], v[180:183], v[16:31]
	ds_read_b128 v[180:183], v192 offset:5120
	s_waitcnt lgkmcnt(2)
	v_mfma_f32_32x32x16_f16 v[0:15], a[252:255], v[184:187], v[0:15]
	ds_read_b128 v[184:187], v192 offset:6144
	v_mfma_f32_32x32x16_f16 v[16:31], a[252:255], v[188:191], v[16:31]
	ds_read_b128 v[188:191], v192 offset:7168
	s_mov_b32 m0, s56
	s_add_u32 s44, s34, 0x10000
	s_addc_u32 s45, s35, 0
	global_load_lds_dwordx4 v192, s[44:45] sc1
	s_nop 3
	global_load_dword v228, v249, s[42:43] offset:0
	global_load_dword v229, v249, s[42:43] offset:256
	s_waitcnt lgkmcnt(2)
	v_mfma_f32_32x32x16_f16 v[32:47], a[0:3], v[160:163], v[32:47]
	ds_read_b128 v[160:163], v192 offset:8192
	v_exp_f32_e32 v200, v0
	v_mfma_f32_32x32x16_f16 v[48:63], a[0:3], v[164:167], v[48:63]
	ds_read_b128 v[164:167], v192 offset:9216
	s_lshl_b32 s64, s71, 3
	s_add_u32 s64, s64, s29
	s_lshl_b32 s64, s64, 7
	s_add_u32 s38, s8, s64
	s_addc_u32 s39, s9, 0
	global_load_dword v251, v196, s[38:39] sc1
	v_exp_f32_e32 v201, v1
	v_add_f32_e32 v200, 1.0, v200
	v_mfma_f32_32x32x16_f16 v[32:47], a[4:7], v[168:171], v[32:47]
	ds_read_b128 v[168:171], v192 offset:10240
	v_exp_f32_e32 v202, v2
	v_add_f32_e32 v201, 1.0, v201
	v_mfma_f32_32x32x16_f16 v[48:63], a[4:7], v[172:175], v[48:63]
	ds_read_b128 v[172:175], v192 offset:11264
	global_load_lds_dwordx4 v192, s[44:45] offset:1024 sc1
	v_exp_f32_e32 v203, v3
	v_add_f32_e32 v202, 1.0, v202
	v_mfma_f32_32x32x16_f16 v[32:47], a[8:11], v[176:179], v[32:47]
	ds_read_b128 v[176:179], v192 offset:12288
	v_exp_f32_e32 v204, v4
	v_add_f32_e32 v203, 1.0, v203
	v_mfma_f32_32x32x16_f16 v[48:63], a[8:11], v[180:183], v[48:63]
	ds_read_b128 v[180:183], v192 offset:13312
	v_exp_f32_e32 v205, v5
	v_add_f32_e32 v204, 1.0, v204
	s_waitcnt lgkmcnt(2)
	v_mfma_f32_32x32x16_f16 v[32:47], a[12:15], v[184:187], v[32:47]
	ds_read_b128 v[184:187], v192 offset:14336
	v_exp_f32_e32 v206, v6
	v_add_f32_e32 v205, 1.0, v205
	v_mfma_f32_32x32x16_f16 v[48:63], a[12:15], v[188:191], v[48:63]
	ds_read_b128 v[188:191], v192 offset:15360
	global_load_lds_dwordx4 v192, s[44:45] offset:2048 sc1
	v_exp_f32_e32 v207, v7
	v_add_f32_e32 v206, 1.0, v206
	v_mfma_f32_32x32x16_f16 v[32:47], a[16:19], v[160:163], v[32:47]
	ds_read_b128 v[160:163], v192 offset:16384
	v_exp_f32_e32 v208, v8
	v_add_f32_e32 v207, 1.0, v207
	v_mfma_f32_32x32x16_f16 v[48:63], a[16:19], v[164:167], v[48:63]
	ds_read_b128 v[164:167], v192 offset:17408
	v_exp_f32_e32 v209, v9
	v_add_f32_e32 v208, 1.0, v208
	v_mfma_f32_32x32x16_f16 v[32:47], a[20:23], v[168:171], v[32:47]
	ds_read_b128 v[168:171], v192 offset:18432
	v_exp_f32_e32 v210, v10
	v_add_f32_e32 v209, 1.0, v209
	v_mfma_f32_32x32x16_f16 v[48:63], a[20:23], v[172:175], v[48:63]
	ds_read_b128 v[172:175], v192 offset:19456
	global_load_lds_dwordx4 v192, s[44:45] offset:3072 sc1
	v_exp_f32_e32 v211, v11
	v_add_f32_e32 v210, 1.0, v210
	s_waitcnt lgkmcnt(2)
	v_mfma_f32_32x32x16_f16 v[32:47], a[24:27], v[176:179], v[32:47]
	ds_read_b128 v[176:179], v192 offset:20480
	v_exp_f32_e32 v212, v12
	v_add_f32_e32 v211, 1.0, v211
	v_mfma_f32_32x32x16_f16 v[48:63], a[24:27], v[180:183], v[48:63]
	ds_read_b128 v[180:183], v192 offset:21504
	v_exp_f32_e32 v213, v13
	v_add_f32_e32 v212, 1.0, v212
	v_mfma_f32_32x32x16_f16 v[32:47], a[28:31], v[184:187], v[32:47]
	ds_read_b128 v[184:187], v192 offset:22528
	v_exp_f32_e32 v214, v14
	v_add_f32_e32 v213, 1.0, v213
	v_mfma_f32_32x32x16_f16 v[48:63], a[28:31], v[188:191], v[48:63]
	ds_read_b128 v[188:191], v192 offset:23552
	s_mov_b32 m0, s57
	s_add_u32 s44, s34, 0x11000
	s_addc_u32 s45, s35, 0
	global_load_lds_dwordx4 v192, s[44:45] sc1
	v_exp_f32_e32 v215, v15
	v_add_f32_e32 v214, 1.0, v214
	v_mfma_f32_32x32x16_f16 v[32:47], a[32:35], v[160:163], v[32:47]
	ds_read_b128 v[160:163], v192 offset:24576
	v_add_f32_e32 v215, 1.0, v215
	v_rcp_f32_e32 v200, v200
	v_mfma_f32_32x32x16_f16 v[48:63], a[32:35], v[164:167], v[48:63]
	ds_read_b128 v[164:167], v192 offset:25600
	v_rcp_f32_e32 v201, v201
	s_waitcnt lgkmcnt(2)
	v_mfma_f32_32x32x16_f16 v[32:47], a[36:39], v[168:171], v[32:47]
	ds_read_b128 v[168:171], v192 offset:26624
	v_rcp_f32_e32 v202, v202
	v_mfma_f32_32x32x16_f16 v[48:63], a[36:39], v[172:175], v[48:63]
	ds_read_b128 v[172:175], v192 offset:27648
	global_load_lds_dwordx4 v192, s[44:45] offset:1024 sc1
	v_rcp_f32_e32 v203, v203
	v_mfma_f32_32x32x16_f16 v[32:47], a[40:43], v[176:179], v[32:47]
	ds_read_b128 v[176:179], v192 offset:28672
	v_rcp_f32_e32 v204, v204
	v_mfma_f32_32x32x16_f16 v[48:63], a[40:43], v[180:183], v[48:63]
	ds_read_b128 v[180:183], v192 offset:29696
	v_rcp_f32_e32 v205, v205
	v_mul_f32_e32 v204, v204, v128
	v_mfma_f32_32x32x16_f16 v[32:47], a[44:47], v[184:187], v[32:47]
	ds_read_b128 v[184:187], v192 offset:30720
	v_rcp_f32_e32 v206, v206
	v_mul_f32_e32 v205, v205, v129
	v_mfma_f32_32x32x16_f16 v[48:63], a[44:47], v[188:191], v[48:63]
	ds_read_b128 v[188:191], v192 offset:31744
	global_load_lds_dwordx4 v192, s[44:45] offset:2048 sc1
	v_rcp_f32_e32 v207, v207
	v_mul_f32_e32 v206, v206, v130
	s_waitcnt vmcnt(10)
	s_barrier
	s_waitcnt lgkmcnt(2)
	v_mfma_f32_32x32x16_f16 v[32:47], a[48:51], v[160:163], v[32:47]
	ds_read_b128 v[160:163], v192 offset:32768
	v_rcp_f32_e32 v208, v208
	v_mul_f32_e32 v207, v207, v131
	v_mfma_f32_32x32x16_f16 v[48:63], a[48:51], v[164:167], v[48:63]
	ds_read_b128 v[164:167], v192 offset:33792
	v_rcp_f32_e32 v209, v209
	v_fmamk_f32 v208, v208, 0xc0b8aa3b, v198
	v_mfma_f32_32x32x16_f16 v[32:47], a[52:55], v[168:171], v[32:47]
	ds_read_b128 v[168:171], v192 offset:34816
	v_rcp_f32_e32 v210, v210
	v_fmamk_f32 v209, v209, 0xc0b8aa3b, v198
	v_fma_f32 v128, v200, v208, v204
	v_mfma_f32_32x32x16_f16 v[48:63], a[52:55], v[172:175], v[48:63]
	ds_read_b128 v[172:175], v192 offset:35840
	global_load_lds_dwordx4 v192, s[44:45] offset:3072 sc1
	v_rcp_f32_e32 v211, v211
	v_fmamk_f32 v210, v210, 0xc0b8aa3b, v198
	v_fma_f32 v129, v201, v209, v205
	v_mfma_f32_32x32x16_f16 v[32:47], a[56:59], v[176:179], v[32:47]
	ds_read_b128 v[176:179], v192 offset:36864
	v_rcp_f32_e32 v212, v212
	v_fmamk_f32 v211, v211, 0xc0b8aa3b, v198
	v_fma_f32 v130, v202, v210, v206
	v_mfma_f32_32x32x16_f16 v[48:63], a[56:59], v[180:183], v[48:63]
	ds_read_b128 v[180:183], v192 offset:37888
	v_rcp_f32_e32 v213, v213
	v_fma_f32 v131, v203, v211, v207
	s_waitcnt lgkmcnt(2)
	v_mfma_f32_32x32x16_f16 v[32:47], a[60:63], v[184:187], v[32:47]
	ds_read_b128 v[184:187], v192 offset:38912
	v_rcp_f32_e32 v214, v214
	v_mfma_f32_32x32x16_f16 v[48:63], a[60:63], v[188:191], v[48:63]
	ds_read_b128 v[188:191], v192 offset:39936
	s_mov_b32 m0, s58
	s_add_u32 s44, s34, 0x18000
	s_addc_u32 s45, s35, 0
	global_load_lds_dwordx4 v192, s[44:45] sc1
	v_rcp_f32_e32 v215, v215
	v_mfma_f32_32x32x16_f16 v[32:47], a[64:67], v[160:163], v[32:47]
	ds_read_b128 v[160:163], v192 offset:40960
	v_exp_f32_e32 v200, v128
	v_mfma_f32_32x32x16_f16 v[48:63], a[64:67], v[164:167], v[48:63]
	ds_read_b128 v[164:167], v192 offset:41984
	v_exp_f32_e32 v201, v129
	v_add_f32_e32 v200, 1.0, v200
	v_mfma_f32_32x32x16_f16 v[32:47], a[68:71], v[168:171], v[32:47]
	ds_read_b128 v[168:171], v192 offset:43008
	v_exp_f32_e32 v202, v130
	v_add_f32_e32 v201, 1.0, v201
	v_mfma_f32_32x32x16_f16 v[48:63], a[68:71], v[172:175], v[48:63]
	ds_read_b128 v[172:175], v192 offset:44032
	global_load_lds_dwordx4 v192, s[44:45] offset:1024 sc1
	v_exp_f32_e32 v203, v131
	v_add_f32_e32 v202, 1.0, v202
	s_waitcnt lgkmcnt(2)
	v_mfma_f32_32x32x16_f16 v[32:47], a[72:75], v[176:179], v[32:47]
	ds_read_b128 v[176:179], v192 offset:45056
	v_add_f32_e32 v203, 1.0, v203
	v_rcp_f32_e32 v200, v200
	v_mfma_f32_32x32x16_f16 v[48:63], a[72:75], v[180:183], v[48:63]
	ds_read_b128 v[180:183], v192 offset:46080
	v_rcp_f32_e32 v201, v201
	v_fma_f32 v200, v200, 2.0, -1.0
	v_mfma_f32_32x32x16_f16 v[32:47], a[76:79], v[184:187], v[32:47]
	ds_read_b128 v[184:187], v192 offset:47104
	v_rcp_f32_e32 v202, v202
	v_fma_f32 v201, v201, 2.0, -1.0
	v_mul_f32_e32 v216, v212, v200
	v_mfma_f32_32x32x16_f16 v[48:63], a[76:79], v[188:191], v[48:63]
	ds_read_b128 v[188:191], v192 offset:48128
	global_load_lds_dwordx4 v192, s[44:45] offset:2048 sc1
	v_rcp_f32_e32 v203, v203
	v_fma_f32 v202, v202, 2.0, -1.0
	v_mul_f32_e32 v217, v213, v201
	v_mfma_f32_32x32x16_f16 v[32:47], a[80:83], v[160:163], v[32:47]
	ds_read_b128 v[160:163], v192 offset:49152
	v_fma_f32 v203, v203, 2.0, -1.0
	v_mul_f32_e32 v218, v214, v202
	v_exp_f32_e32 v200, v16
	v_mfma_f32_32x32x16_f16 v[48:63], a[80:83], v[164:167], v[48:63]
	ds_read_b128 v[164:167], v192 offset:50176
	v_mul_f32_e32 v219, v215, v203
	v_cvt_pk_f16_f32 v220, v216, v217
	v_exp_f32_e32 v201, v17
	s_waitcnt lgkmcnt(2)
	v_mfma_f32_32x32x16_f16 v[32:47], a[84:87], v[168:171], v[32:47]
	ds_read_b128 v[168:171], v192 offset:51200
	v_cvt_pk_f16_f32 v221, v218, v219
	v_exp_f32_e32 v202, v18
	v_add_f32_e32 v200, 1.0, v200
	v_mfma_f32_32x32x16_f16 v[48:63], a[84:87], v[172:175], v[48:63]
	ds_read_b128 v[172:175], v192 offset:52224
	global_load_lds_dwordx4 v192, s[44:45] offset:3072 sc1
	s_cmp_eq_u32 s33, s60
	s_cbranch_scc1 .LE_ht22

.LE_join29:
	v_mfma_f32_32x32x16_f16 v[48:63], a[168:171], v[180:183], v[48:63]
	ds_read_b128 v[180:183], v193 offset:29696
	v_mfma_f32_32x32x16_f16 v[32:47], a[172:175], v[184:187], v[32:47]
	ds_read_b128 v[184:187], v193 offset:30720
	v_mfma_f32_32x32x16_f16 v[48:63], a[172:175], v[188:191], v[48:63]
	ds_read_b128 v[188:191], v193 offset:31744
	global_load_lds_dwordx4 v192, s[44:45] offset:2048 sc1
	s_waitcnt vmcnt(8)
	s_barrier
	v_mfma_f32_32x32x16_f16 v[32:47], a[176:179], v[160:163], v[32:47]
	ds_read_b128 v[160:163], v193 offset:32768
	v_mfma_f32_32x32x16_f16 v[48:63], a[176:179], v[164:167], v[48:63]
	ds_read_b128 v[164:167], v193 offset:33792
	s_waitcnt lgkmcnt(2)
	v_mfma_f32_32x32x16_f16 v[32:47], a[180:183], v[168:171], v[32:47]
	ds_read_b128 v[168:171], v193 offset:34816
	v_mfma_f32_32x32x16_f16 v[48:63], a[180:183], v[172:175], v[48:63]
	ds_read_b128 v[172:175], v193 offset:35840
	global_load_lds_dwordx4 v192, s[44:45] offset:3072 sc1
	v_mfma_f32_32x32x16_f16 v[32:47], a[184:187], v[176:179], v[32:47]
	ds_read_b128 v[176:179], v193 offset:36864
	v_mfma_f32_32x32x16_f16 v[48:63], a[184:187], v[180:183], v[48:63]
	ds_read_b128 v[180:183], v193 offset:37888
	v_mfma_f32_32x32x16_f16 v[32:47], a[188:191], v[184:187], v[32:47]
	ds_read_b128 v[184:187], v193 offset:38912
	v_mfma_f32_32x32x16_f16 v[48:63], a[188:191], v[188:191], v[48:63]
	ds_read_b128 v[188:191], v193 offset:39936
	s_mov_b32 m0, s54
	s_add_u32 s44, s34, 0x8000
	s_addc_u32 s45, s35, 0
	global_load_lds_dwordx4 v192, s[44:45] sc1
	s_waitcnt lgkmcnt(2)
	v_mfma_f32_32x32x16_f16 v[32:47], a[192:195], v[160:163], v[32:47]
	ds_read_b128 v[160:163], v193 offset:40960
	v_mfma_f32_32x32x16_f16 v[48:63], a[192:195], v[164:167], v[48:63]
	ds_read_b128 v[164:167], v193 offset:41984
	v_mfma_f32_32x32x16_f16 v[32:47], a[196:199], v[168:171], v[32:47]
	ds_read_b128 v[168:171], v193 offset:43008
	v_mfma_f32_32x32x16_f16 v[48:63], a[196:199], v[172:175], v[48:63]
	ds_read_b128 v[172:175], v193 offset:44032
	global_load_lds_dwordx4 v192, s[44:45] offset:1024 sc1
	v_mfma_f32_32x32x16_f16 v[32:47], a[200:203], v[176:179], v[32:47]
	ds_read_b128 v[176:179], v193 offset:45056
	v_mfma_f32_32x32x16_f16 v[48:63], a[200:203], v[180:183], v[48:63]
	ds_read_b128 v[180:183], v193 offset:46080
	s_waitcnt lgkmcnt(2)
	v_mfma_f32_32x32x16_f16 v[32:47], a[204:207], v[184:187], v[32:47]
	ds_read_b128 v[184:187], v193 offset:47104
	v_mfma_f32_32x32x16_f16 v[48:63], a[204:207], v[188:191], v[48:63]
	ds_read_b128 v[188:191], v193 offset:48128
	global_load_lds_dwordx4 v192, s[44:45] offset:2048 sc1
	v_mfma_f32_32x32x16_f16 v[32:47], a[208:211], v[160:163], v[32:47]
	ds_read_b128 v[160:163], v193 offset:49152
	v_mfma_f32_32x32x16_f16 v[48:63], a[208:211], v[164:167], v[48:63]
	ds_read_b128 v[164:167], v193 offset:50176
	s_waitcnt vmcnt(5)
	s_barrier
	v_mov_b32_e32 v199, 1
	s_cmp_eq_u32 s31, 0
	s_cbranch_scc1 .LE_slow30
	global_store_dword v197, v199, s[40:41]
.LE_join31:
	v_mfma_f32_32x32x16_f16 v[32:47], a[212:215], v[168:171], v[32:47]
	ds_read_b128 v[168:171], v193 offset:51200
	v_mfma_f32_32x32x16_f16 v[48:63], a[212:215], v[172:175], v[48:63]
	ds_read_b128 v[172:175], v193 offset:52224
	global_load_lds_dwordx4 v192, s[44:45] offset:3072 sc1
	s_waitcnt lgkmcnt(2)
	v_mfma_f32_32x32x16_f16 v[32:47], a[216:219], v[176:179], v[32:47]
	ds_read_b128 v[176:179], v193 offset:53248
	v_mfma_f32_32x32x16_f16 v[48:63], a[216:219], v[180:183], v[48:63]
	ds_read_b128 v[180:183], v193 offset:54272
	s_and_b32 s64, s33, 1
	s_lshl_b32 s64, s64, 22
	s_add_u32 s64, s64, s50
	s_add_u32 s64, s64, 0x20000
	s_add_u32 s36, s6, s64
	s_addc_u32 s37, s7, 0
	s_lshl_b32 s64, s33, 3
	s_add_u32 s64, s64, s29
	s_lshl_b32 s64, s64, 5
	s_add_u32 s64, s64, s30
	s_lshl_b32 s64, s64, 2
	s_add_u32 s40, s8, s64
	s_addc_u32 s41, s9, 0
	s_lshl_b32 s64, s61, 11
	s_lshl_b32 s65, s29, 8
	s_add_u32 s64, s64, s65
	s_lshl_b32 s64, s64, 3
	s_add_u32 s42, s12, s64
	s_addc_u32 s43, s13, 0
	v_mfma_f32_32x32x16_f16 v[32:47], a[220:223], v[184:187], v[32:47]
	ds_read_b128 v[184:187], v193 offset:55296
	v_mfma_f32_32x32x16_f16 v[48:63], a[220:223], v[188:191], v[48:63]
	ds_read_b128 v[188:191], v193 offset:56320
	s_mov_b32 m0, s55
	s_add_u32 s44, s34, 0x9000
	s_addc_u32 s45, s35, 0
	global_load_lds_dwordx4 v192, s[44:45] sc1
	v_mfma_f32_32x32x16_f16 v[32:47], a[224:227], v[160:163], v[32:47]
	ds_read_b128 v[160:163], v193 offset:57344
	v_mfma_f32_32x32x16_f16 v[48:63], a[224:227], v[164:167], v[48:63]
	ds_read_b128 v[164:167], v193 offset:58368
	s_waitcnt lgkmcnt(2)
	v_mfma_f32_32x32x16_f16 v[32:47], a[228:231], v[168:171], v[32:47]
	ds_read_b128 v[168:171], v193 offset:59392
	v_mfma_f32_32x32x16_f16 v[48:63], a[228:231], v[172:175], v[48:63]
	ds_read_b128 v[172:175], v193 offset:60416
	global_load_lds_dwordx4 v192, s[44:45] offset:1024 sc1
	v_mfma_f32_32x32x16_f16 v[32:47], a[232:235], v[176:179], v[32:47]
	ds_read_b128 v[176:179], v193 offset:61440
	v_mfma_f32_32x32x16_f16 v[48:63], a[232:235], v[180:183], v[48:63]
	ds_read_b128 v[180:183], v193 offset:62464
	v_mfma_f32_32x32x16_f16 v[32:47], a[236:239], v[184:187], v[32:47]
	ds_read_b128 v[184:187], v193 offset:63488
	v_mfma_f32_32x32x16_f16 v[48:63], a[236:239], v[188:191], v[48:63]
	ds_read_b128 v[188:191], v193 offset:64512
	global_load_lds_dwordx4 v192, s[44:45] offset:2048 sc1
	s_waitcnt vmcnt(8)
	s_barrier
	s_waitcnt lgkmcnt(2)
	v_mfma_f32_32x32x16_f16 v[32:47], a[240:243], v[160:163], v[32:47]
	ds_read_b128 v[160:163], v192 offset:0
	v_mfma_f32_32x32x16_f16 v[48:63], a[240:243], v[164:167], v[48:63]
	ds_read_b128 v[164:167], v192 offset:1024
	v_mfma_f32_32x32x16_f16 v[32:47], a[244:247], v[168:171], v[32:47]
	ds_read_b128 v[168:171], v192 offset:2048
	v_mfma_f32_32x32x16_f16 v[48:63], a[244:247], v[172:175], v[48:63]
	ds_read_b128 v[172:175], v192 offset:3072
	global_load_lds_dwordx4 v192, s[44:45] offset:3072 sc1
	v_mfma_f32_32x32x16_f16 v[32:47], a[248:251], v[176:179], v[32:47]
	ds_read_b128 v[176:179], v192 offset:4096
	v_mfma_f32_32x32x16_f16 v[48:63], a[248:251], v[180:183], v[48:63]
	ds_read_b128 v[180:183], v192 offset:5120
	s_waitcnt lgkmcnt(2)
	v_mfma_f32_32x32x16_f16 v[32:47], a[252:255], v[184:187], v[32:47]
	ds_read_b128 v[184:187], v192 offset:6144
	v_mfma_f32_32x32x16_f16 v[48:63], a[252:255], v[188:191], v[48:63]
	ds_read_b128 v[188:191], v192 offset:7168
	s_mov_b32 m0, s56
	s_add_u32 s44, s34, 0x10000
	s_addc_u32 s45, s35, 0
	global_load_lds_dwordx4 v192, s[44:45] sc1
	s_nop 3
	global_load_dword v228, v249, s[42:43] offset:0
	global_load_dword v229, v249, s[42:43] offset:256
	s_waitcnt lgkmcnt(2)
	v_mfma_f32_32x32x16_f16 v[64:79], a[0:3], v[160:163], v[64:79]
	ds_read_b128 v[160:163], v192 offset:8192
	v_exp_f32_e32 v200, v32
	v_mfma_f32_32x32x16_f16 v[80:95], a[0:3], v[164:167], v[80:95]
	ds_read_b128 v[164:167], v192 offset:9216
	s_lshl_b32 s64, s71, 3
	s_add_u32 s64, s64, s29
	s_lshl_b32 s64, s64, 7
	s_add_u32 s38, s8, s64
	s_addc_u32 s39, s9, 0
	global_load_dword v251, v196, s[38:39] sc1
	v_exp_f32_e32 v201, v33
	v_add_f32_e32 v200, 1.0, v200
	v_mfma_f32_32x32x16_f16 v[64:79], a[4:7], v[168:171], v[64:79]
	ds_read_b128 v[168:171], v192 offset:10240
	v_exp_f32_e32 v202, v34
	v_add_f32_e32 v201, 1.0, v201
	v_mfma_f32_32x32x16_f16 v[80:95], a[4:7], v[172:175], v[80:95]
	ds_read_b128 v[172:175], v192 offset:11264
	global_load_lds_dwordx4 v192, s[44:45] offset:1024 sc1
	v_exp_f32_e32 v203, v35
	v_add_f32_e32 v202, 1.0, v202
	v_mfma_f32_32x32x16_f16 v[64:79], a[8:11], v[176:179], v[64:79]
	ds_read_b128 v[176:179], v192 offset:12288
	v_exp_f32_e32 v204, v36
	v_add_f32_e32 v203, 1.0, v203
	v_mfma_f32_32x32x16_f16 v[80:95], a[8:11], v[180:183], v[80:95]
	ds_read_b128 v[180:183], v192 offset:13312
	v_exp_f32_e32 v205, v37
	v_add_f32_e32 v204, 1.0, v204
	s_waitcnt lgkmcnt(2)
	v_mfma_f32_32x32x16_f16 v[64:79], a[12:15], v[184:187], v[64:79]
	ds_read_b128 v[184:187], v192 offset:14336
	v_exp_f32_e32 v206, v38
	v_add_f32_e32 v205, 1.0, v205
	v_mfma_f32_32x32x16_f16 v[80:95], a[12:15], v[188:191], v[80:95]
	ds_read_b128 v[188:191], v192 offset:15360
	global_load_lds_dwordx4 v192, s[44:45] offset:2048 sc1
	v_exp_f32_e32 v207, v39
	v_add_f32_e32 v206, 1.0, v206
	v_mfma_f32_32x32x16_f16 v[64:79], a[16:19], v[160:163], v[64:79]
	ds_read_b128 v[160:163], v192 offset:16384
	v_exp_f32_e32 v208, v40
	v_add_f32_e32 v207, 1.0, v207
	v_mfma_f32_32x32x16_f16 v[80:95], a[16:19], v[164:167], v[80:95]
	ds_read_b128 v[164:167], v192 offset:17408
	v_exp_f32_e32 v209, v41
	v_add_f32_e32 v208, 1.0, v208
	v_mfma_f32_32x32x16_f16 v[64:79], a[20:23], v[168:171], v[64:79]
	ds_read_b128 v[168:171], v192 offset:18432
	v_exp_f32_e32 v210, v42
	v_add_f32_e32 v209, 1.0, v209
	v_mfma_f32_32x32x16_f16 v[80:95], a[20:23], v[172:175], v[80:95]
	ds_read_b128 v[172:175], v192 offset:19456
	global_load_lds_dwordx4 v192, s[44:45] offset:3072 sc1
	v_exp_f32_e32 v211, v43
	v_add_f32_e32 v210, 1.0, v210
	s_waitcnt lgkmcnt(2)
	v_mfma_f32_32x32x16_f16 v[64:79], a[24:27], v[176:179], v[64:79]
	ds_read_b128 v[176:179], v192 offset:20480
	v_exp_f32_e32 v212, v44
	v_add_f32_e32 v211, 1.0, v211
	v_mfma_f32_32x32x16_f16 v[80:95], a[24:27], v[180:183], v[80:95]
	ds_read_b128 v[180:183], v192 offset:21504
	v_exp_f32_e32 v213, v45
	v_add_f32_e32 v212, 1.0, v212
	v_mfma_f32_32x32x16_f16 v[64:79], a[28:31], v[184:187], v[64:79]
	ds_read_b128 v[184:187], v192 offset:22528
	v_exp_f32_e32 v214, v46
	v_add_f32_e32 v213, 1.0, v213
	v_mfma_f32_32x32x16_f16 v[80:95], a[28:31], v[188:191], v[80:95]
	ds_read_b128 v[188:191], v192 offset:23552
	s_mov_b32 m0, s57
	s_add_u32 s44, s34, 0x11000
	s_addc_u32 s45, s35, 0
	global_load_lds_dwordx4 v192, s[44:45] sc1
	v_exp_f32_e32 v215, v47
	v_add_f32_e32 v214, 1.0, v214
	v_mfma_f32_32x32x16_f16 v[64:79], a[32:35], v[160:163], v[64:79]
	ds_read_b128 v[160:163], v192 offset:24576
	v_add_f32_e32 v215, 1.0, v215
	v_rcp_f32_e32 v200, v200
	v_mfma_f32_32x32x16_f16 v[80:95], a[32:35], v[164:167], v[80:95]
	ds_read_b128 v[164:167], v192 offset:25600
	v_rcp_f32_e32 v201, v201
	s_waitcnt lgkmcnt(2)
	v_mfma_f32_32x32x16_f16 v[64:79], a[36:39], v[168:171], v[64:79]
	ds_read_b128 v[168:171], v192 offset:26624
	v_rcp_f32_e32 v202, v202
	v_mfma_f32_32x32x16_f16 v[80:95], a[36:39], v[172:175], v[80:95]
	ds_read_b128 v[172:175], v192 offset:27648
	global_load_lds_dwordx4 v192, s[44:45] offset:1024 sc1
	v_rcp_f32_e32 v203, v203
	v_mfma_f32_32x32x16_f16 v[64:79], a[40:43], v[176:179], v[64:79]
	ds_read_b128 v[176:179], v192 offset:28672
	v_rcp_f32_e32 v204, v204
	v_mfma_f32_32x32x16_f16 v[80:95], a[40:43], v[180:183], v[80:95]
	ds_read_b128 v[180:183], v192 offset:29696
	v_rcp_f32_e32 v205, v205
	v_mul_f32_e32 v204, v204, v136
	v_mfma_f32_32x32x16_f16 v[64:79], a[44:47], v[184:187], v[64:79]
	ds_read_b128 v[184:187], v192 offset:30720
	v_rcp_f32_e32 v206, v206
	v_mul_f32_e32 v205, v205, v137
	v_mfma_f32_32x32x16_f16 v[80:95], a[44:47], v[188:191], v[80:95]
	ds_read_b128 v[188:191], v192 offset:31744
	global_load_lds_dwordx4 v192, s[44:45] offset:2048 sc1
	v_rcp_f32_e32 v207, v207
	v_mul_f32_e32 v206, v206, v138
	s_waitcnt vmcnt(10)
	s_barrier
	s_waitcnt lgkmcnt(2)
	v_mfma_f32_32x32x16_f16 v[64:79], a[48:51], v[160:163], v[64:79]
	ds_read_b128 v[160:163], v192 offset:32768
	v_rcp_f32_e32 v208, v208
	v_mul_f32_e32 v207, v207, v139
	v_mfma_f32_32x32x16_f16 v[80:95], a[48:51], v[164:167], v[80:95]
	ds_read_b128 v[164:167], v192 offset:33792
	v_rcp_f32_e32 v209, v209
	v_fmamk_f32 v208, v208, 0xc0b8aa3b, v198
	v_mfma_f32_32x32x16_f16 v[64:79], a[52:55], v[168:171], v[64:79]
	ds_read_b128 v[168:171], v192 offset:34816
	v_rcp_f32_e32 v210, v210
	v_fmamk_f32 v209, v209, 0xc0b8aa3b, v198
	v_fma_f32 v136, v200, v208, v204
	v_mfma_f32_32x32x16_f16 v[80:95], a[52:55], v[172:175], v[80:95]
	ds_read_b128 v[172:175], v192 offset:35840
	global_load_lds_dwordx4 v192, s[44:45] offset:3072 sc1
	v_rcp_f32_e32 v211, v211
	v_fmamk_f32 v210, v210, 0xc0b8aa3b, v198
	v_fma_f32 v137, v201, v209, v205
	v_mfma_f32_32x32x16_f16 v[64:79], a[56:59], v[176:179], v[64:79]
	ds_read_b128 v[176:179], v192 offset:36864
	v_rcp_f32_e32 v212, v212
	v_fmamk_f32 v211, v211, 0xc0b8aa3b, v198
	v_fma_f32 v138, v202, v210, v206
	v_mfma_f32_32x32x16_f16 v[80:95], a[56:59], v[180:183], v[80:95]
	ds_read_b128 v[180:183], v192 offset:37888
	v_rcp_f32_e32 v213, v213
	v_fma_f32 v139, v203, v211, v207
	s_waitcnt lgkmcnt(2)
	v_mfma_f32_32x32x16_f16 v[64:79], a[60:63], v[184:187], v[64:79]
	ds_read_b128 v[184:187], v192 offset:38912
	v_rcp_f32_e32 v214, v214
	v_mfma_f32_32x32x16_f16 v[80:95], a[60:63], v[188:191], v[80:95]
	ds_read_b128 v[188:191], v192 offset:39936
	s_mov_b32 m0, s58
	s_add_u32 s44, s34, 0x18000
	s_addc_u32 s45, s35, 0
	global_load_lds_dwordx4 v192, s[44:45] sc1
	v_rcp_f32_e32 v215, v215
	v_mfma_f32_32x32x16_f16 v[64:79], a[64:67], v[160:163], v[64:79]
	ds_read_b128 v[160:163], v192 offset:40960
	v_exp_f32_e32 v200, v136
	v_mfma_f32_32x32x16_f16 v[80:95], a[64:67], v[164:167], v[80:95]
	ds_read_b128 v[164:167], v192 offset:41984
	v_exp_f32_e32 v201, v137
	v_add_f32_e32 v200, 1.0, v200
	v_mfma_f32_32x32x16_f16 v[64:79], a[68:71], v[168:171], v[64:79]
	ds_read_b128 v[168:171], v192 offset:43008
	v_exp_f32_e32 v202, v138
	v_add_f32_e32 v201, 1.0, v201
	v_mfma_f32_32x32x16_f16 v[80:95], a[68:71], v[172:175], v[80:95]
	ds_read_b128 v[172:175], v192 offset:44032
	global_load_lds_dwordx4 v192, s[44:45] offset:1024 sc1
	v_exp_f32_e32 v203, v139
	v_add_f32_e32 v202, 1.0, v202
	s_waitcnt lgkmcnt(2)
	v_mfma_f32_32x32x16_f16 v[64:79], a[72:75], v[176:179], v[64:79]
	ds_read_b128 v[176:179], v192 offset:45056
	v_add_f32_e32 v203, 1.0, v203
	v_rcp_f32_e32 v200, v200
	v_mfma_f32_32x32x16_f16 v[80:95], a[72:75], v[180:183], v[80:95]
	ds_read_b128 v[180:183], v192 offset:46080
	v_rcp_f32_e32 v201, v201
	v_fma_f32 v200, v200, 2.0, -1.0
	v_mfma_f32_32x32x16_f16 v[64:79], a[76:79], v[184:187], v[64:79]
	ds_read_b128 v[184:187], v192 offset:47104
	v_rcp_f32_e32 v202, v202
	v_fma_f32 v201, v201, 2.0, -1.0
	v_mul_f32_e32 v216, v212, v200
	v_mfma_f32_32x32x16_f16 v[80:95], a[76:79], v[188:191], v[80:95]
	ds_read_b128 v[188:191], v192 offset:48128
	global_load_lds_dwordx4 v192, s[44:45] offset:2048 sc1
	v_rcp_f32_e32 v203, v203
	v_fma_f32 v202, v202, 2.0, -1.0
	v_mul_f32_e32 v217, v213, v201
	v_mfma_f32_32x32x16_f16 v[64:79], a[80:83], v[160:163], v[64:79]
	ds_read_b128 v[160:163], v192 offset:49152
	v_fma_f32 v203, v203, 2.0, -1.0
	v_mul_f32_e32 v218, v214, v202
	v_exp_f32_e32 v200, v48
	v_mfma_f32_32x32x16_f16 v[80:95], a[80:83], v[164:167], v[80:95]
	ds_read_b128 v[164:167], v192 offset:50176
	v_mul_f32_e32 v219, v215, v203
	v_cvt_pk_f16_f32 v220, v216, v217
	v_exp_f32_e32 v201, v49
	s_waitcnt lgkmcnt(2)
	v_mfma_f32_32x32x16_f16 v[64:79], a[84:87], v[168:171], v[64:79]
	ds_read_b128 v[168:171], v192 offset:51200
	v_cvt_pk_f16_f32 v221, v218, v219
	v_exp_f32_e32 v202, v50
	v_add_f32_e32 v200, 1.0, v200
	v_mfma_f32_32x32x16_f16 v[80:95], a[84:87], v[172:175], v[80:95]
	ds_read_b128 v[172:175], v192 offset:52224
	global_load_lds_dwordx4 v192, s[44:45] offset:3072 sc1
	s_cmp_eq_u32 s33, s60
	s_cbranch_scc1 .LE_ht32

.LE_join39:
	v_mfma_f32_32x32x16_f16 v[80:95], a[168:171], v[180:183], v[80:95]
	ds_read_b128 v[180:183], v193 offset:29696
	v_mfma_f32_32x32x16_f16 v[64:79], a[172:175], v[184:187], v[64:79]
	ds_read_b128 v[184:187], v193 offset:30720
	v_mfma_f32_32x32x16_f16 v[80:95], a[172:175], v[188:191], v[80:95]
	ds_read_b128 v[188:191], v193 offset:31744
	global_load_lds_dwordx4 v192, s[44:45] offset:2048 sc1
	s_waitcnt vmcnt(8)
	s_barrier
	v_mfma_f32_32x32x16_f16 v[64:79], a[176:179], v[160:163], v[64:79]
	ds_read_b128 v[160:163], v193 offset:32768
	v_mfma_f32_32x32x16_f16 v[80:95], a[176:179], v[164:167], v[80:95]
	ds_read_b128 v[164:167], v193 offset:33792
	s_waitcnt lgkmcnt(2)
	v_mfma_f32_32x32x16_f16 v[64:79], a[180:183], v[168:171], v[64:79]
	ds_read_b128 v[168:171], v193 offset:34816
	v_mfma_f32_32x32x16_f16 v[80:95], a[180:183], v[172:175], v[80:95]
	ds_read_b128 v[172:175], v193 offset:35840
	global_load_lds_dwordx4 v192, s[44:45] offset:3072 sc1
	v_mfma_f32_32x32x16_f16 v[64:79], a[184:187], v[176:179], v[64:79]
	ds_read_b128 v[176:179], v193 offset:36864
	v_mfma_f32_32x32x16_f16 v[80:95], a[184:187], v[180:183], v[80:95]
	ds_read_b128 v[180:183], v193 offset:37888
	v_mfma_f32_32x32x16_f16 v[64:79], a[188:191], v[184:187], v[64:79]
	ds_read_b128 v[184:187], v193 offset:38912
	v_mfma_f32_32x32x16_f16 v[80:95], a[188:191], v[188:191], v[80:95]
	ds_read_b128 v[188:191], v193 offset:39936
	s_mov_b32 m0, s54
	s_add_u32 s44, s34, 0x8000
	s_addc_u32 s45, s35, 0
	global_load_lds_dwordx4 v192, s[44:45] sc1
	s_waitcnt lgkmcnt(2)
	v_mfma_f32_32x32x16_f16 v[64:79], a[192:195], v[160:163], v[64:79]
	ds_read_b128 v[160:163], v193 offset:40960
	v_mfma_f32_32x32x16_f16 v[80:95], a[192:195], v[164:167], v[80:95]
	ds_read_b128 v[164:167], v193 offset:41984
	v_mfma_f32_32x32x16_f16 v[64:79], a[196:199], v[168:171], v[64:79]
	ds_read_b128 v[168:171], v193 offset:43008
	v_mfma_f32_32x32x16_f16 v[80:95], a[196:199], v[172:175], v[80:95]
	ds_read_b128 v[172:175], v193 offset:44032
	global_load_lds_dwordx4 v192, s[44:45] offset:1024 sc1
	v_mfma_f32_32x32x16_f16 v[64:79], a[200:203], v[176:179], v[64:79]
	ds_read_b128 v[176:179], v193 offset:45056
	v_mfma_f32_32x32x16_f16 v[80:95], a[200:203], v[180:183], v[80:95]
	ds_read_b128 v[180:183], v193 offset:46080
	s_waitcnt lgkmcnt(2)
	v_mfma_f32_32x32x16_f16 v[64:79], a[204:207], v[184:187], v[64:79]
	ds_read_b128 v[184:187], v193 offset:47104
	v_mfma_f32_32x32x16_f16 v[80:95], a[204:207], v[188:191], v[80:95]
	ds_read_b128 v[188:191], v193 offset:48128
	global_load_lds_dwordx4 v192, s[44:45] offset:2048 sc1
	v_mfma_f32_32x32x16_f16 v[64:79], a[208:211], v[160:163], v[64:79]
	ds_read_b128 v[160:163], v193 offset:49152
	v_mfma_f32_32x32x16_f16 v[80:95], a[208:211], v[164:167], v[80:95]
	ds_read_b128 v[164:167], v193 offset:50176
	s_waitcnt vmcnt(5)
	s_barrier
	v_mov_b32_e32 v199, 2
	s_cmp_eq_u32 s31, 0
	s_cbranch_scc1 .LE_slow40
	global_store_dword v197, v199, s[40:41]
.LE_join41:
	v_mfma_f32_32x32x16_f16 v[64:79], a[212:215], v[168:171], v[64:79]
	ds_read_b128 v[168:171], v193 offset:51200
	v_mfma_f32_32x32x16_f16 v[80:95], a[212:215], v[172:175], v[80:95]
	ds_read_b128 v[172:175], v193 offset:52224
	global_load_lds_dwordx4 v192, s[44:45] offset:3072 sc1
	s_waitcnt lgkmcnt(2)
	v_mfma_f32_32x32x16_f16 v[64:79], a[216:219], v[176:179], v[64:79]
	ds_read_b128 v[176:179], v193 offset:53248
	v_mfma_f32_32x32x16_f16 v[80:95], a[216:219], v[180:183], v[80:95]
	ds_read_b128 v[180:183], v193 offset:54272
	s_and_b32 s64, s33, 1
	s_lshl_b32 s64, s64, 22
	s_add_u32 s64, s64, s50
	s_add_u32 s64, s64, 0x40000
	s_add_u32 s36, s6, s64
	s_addc_u32 s37, s7, 0
	s_lshl_b32 s64, s33, 3
	s_add_u32 s64, s64, s29
	s_lshl_b32 s64, s64, 5
	s_add_u32 s64, s64, s30
	s_lshl_b32 s64, s64, 2
	s_add_u32 s40, s8, s64
	s_addc_u32 s41, s9, 0
	s_lshl_b32 s64, s61, 11
	s_lshl_b32 s65, s29, 8
	s_add_u32 s64, s64, s65
	s_add_u32 s64, s64, 64
	s_lshl_b32 s64, s64, 3
	s_add_u32 s42, s12, s64
	s_addc_u32 s43, s13, 0
	v_mfma_f32_32x32x16_f16 v[64:79], a[220:223], v[184:187], v[64:79]
	ds_read_b128 v[184:187], v193 offset:55296
	v_mfma_f32_32x32x16_f16 v[80:95], a[220:223], v[188:191], v[80:95]
	ds_read_b128 v[188:191], v193 offset:56320
	s_mov_b32 m0, s55
	s_add_u32 s44, s34, 0x9000
	s_addc_u32 s45, s35, 0
	global_load_lds_dwordx4 v192, s[44:45] sc1
	v_mfma_f32_32x32x16_f16 v[64:79], a[224:227], v[160:163], v[64:79]
	ds_read_b128 v[160:163], v193 offset:57344
	v_mfma_f32_32x32x16_f16 v[80:95], a[224:227], v[164:167], v[80:95]
	ds_read_b128 v[164:167], v193 offset:58368
	s_waitcnt lgkmcnt(2)
	v_mfma_f32_32x32x16_f16 v[64:79], a[228:231], v[168:171], v[64:79]
	ds_read_b128 v[168:171], v193 offset:59392
	v_mfma_f32_32x32x16_f16 v[80:95], a[228:231], v[172:175], v[80:95]
	ds_read_b128 v[172:175], v193 offset:60416
	global_load_lds_dwordx4 v192, s[44:45] offset:1024 sc1
	v_mfma_f32_32x32x16_f16 v[64:79], a[232:235], v[176:179], v[64:79]
	ds_read_b128 v[176:179], v193 offset:61440
	v_mfma_f32_32x32x16_f16 v[80:95], a[232:235], v[180:183], v[80:95]
	ds_read_b128 v[180:183], v193 offset:62464
	v_mfma_f32_32x32x16_f16 v[64:79], a[236:239], v[184:187], v[64:79]
	ds_read_b128 v[184:187], v193 offset:63488
	v_mfma_f32_32x32x16_f16 v[80:95], a[236:239], v[188:191], v[80:95]
	ds_read_b128 v[188:191], v193 offset:64512
	global_load_lds_dwordx4 v192, s[44:45] offset:2048 sc1
	s_waitcnt vmcnt(8)
	s_barrier
	s_waitcnt lgkmcnt(2)
	v_mfma_f32_32x32x16_f16 v[64:79], a[240:243], v[160:163], v[64:79]
	ds_read_b128 v[160:163], v192 offset:0
	v_mfma_f32_32x32x16_f16 v[80:95], a[240:243], v[164:167], v[80:95]
	ds_read_b128 v[164:167], v192 offset:1024
	v_mfma_f32_32x32x16_f16 v[64:79], a[244:247], v[168:171], v[64:79]
	ds_read_b128 v[168:171], v192 offset:2048
	v_mfma_f32_32x32x16_f16 v[80:95], a[244:247], v[172:175], v[80:95]
	ds_read_b128 v[172:175], v192 offset:3072
	global_load_lds_dwordx4 v192, s[44:45] offset:3072 sc1
	v_mfma_f32_32x32x16_f16 v[64:79], a[248:251], v[176:179], v[64:79]
	ds_read_b128 v[176:179], v192 offset:4096
	v_mfma_f32_32x32x16_f16 v[80:95], a[248:251], v[180:183], v[80:95]
	ds_read_b128 v[180:183], v192 offset:5120
	s_waitcnt lgkmcnt(2)
	v_mfma_f32_32x32x16_f16 v[64:79], a[252:255], v[184:187], v[64:79]
	ds_read_b128 v[184:187], v192 offset:6144
	v_mfma_f32_32x32x16_f16 v[80:95], a[252:255], v[188:191], v[80:95]
	ds_read_b128 v[188:191], v192 offset:7168
	s_mov_b32 m0, s56
	s_add_u32 s44, s34, 0x10000
	s_addc_u32 s45, s35, 0
	global_load_lds_dwordx4 v192, s[44:45] sc1
	s_nop 3
	global_load_dword v228, v249, s[42:43] offset:0
	global_load_dword v229, v249, s[42:43] offset:256
	s_waitcnt lgkmcnt(2)
	v_mfma_f32_32x32x16_f16 v[96:111], a[0:3], v[160:163], v[96:111]
	ds_read_b128 v[160:163], v192 offset:8192
	v_exp_f32_e32 v200, v64
	v_mfma_f32_32x32x16_f16 v[112:127], a[0:3], v[164:167], v[112:127]
	ds_read_b128 v[164:167], v192 offset:9216
	s_lshl_b32 s64, s33, 3
	s_add_u32 s64, s64, s29
	s_lshl_b32 s64, s64, 7
	s_add_u32 s38, s8, s64
	s_addc_u32 s39, s9, 0
	global_load_dword v251, v196, s[38:39] sc1
	v_exp_f32_e32 v201, v65
	v_add_f32_e32 v200, 1.0, v200
	v_mfma_f32_32x32x16_f16 v[96:111], a[4:7], v[168:171], v[96:111]
	ds_read_b128 v[168:171], v192 offset:10240
	v_exp_f32_e32 v202, v66
	v_add_f32_e32 v201, 1.0, v201
	v_mfma_f32_32x32x16_f16 v[112:127], a[4:7], v[172:175], v[112:127]
	ds_read_b128 v[172:175], v192 offset:11264
	global_load_lds_dwordx4 v192, s[44:45] offset:1024 sc1
	v_exp_f32_e32 v203, v67
	v_add_f32_e32 v202, 1.0, v202
	v_mfma_f32_32x32x16_f16 v[96:111], a[8:11], v[176:179], v[96:111]
	ds_read_b128 v[176:179], v192 offset:12288
	v_exp_f32_e32 v204, v68
	v_add_f32_e32 v203, 1.0, v203
	v_mfma_f32_32x32x16_f16 v[112:127], a[8:11], v[180:183], v[112:127]
	ds_read_b128 v[180:183], v192 offset:13312
	v_exp_f32_e32 v205, v69
	v_add_f32_e32 v204, 1.0, v204
	s_waitcnt lgkmcnt(2)
	v_mfma_f32_32x32x16_f16 v[96:111], a[12:15], v[184:187], v[96:111]
	ds_read_b128 v[184:187], v192 offset:14336
	v_exp_f32_e32 v206, v70
	v_add_f32_e32 v205, 1.0, v205
	v_mfma_f32_32x32x16_f16 v[112:127], a[12:15], v[188:191], v[112:127]
	ds_read_b128 v[188:191], v192 offset:15360
	global_load_lds_dwordx4 v192, s[44:45] offset:2048 sc1
	v_exp_f32_e32 v207, v71
	v_add_f32_e32 v206, 1.0, v206
	v_mfma_f32_32x32x16_f16 v[96:111], a[16:19], v[160:163], v[96:111]
	ds_read_b128 v[160:163], v192 offset:16384
	v_exp_f32_e32 v208, v72
	v_add_f32_e32 v207, 1.0, v207
	v_mfma_f32_32x32x16_f16 v[112:127], a[16:19], v[164:167], v[112:127]
	ds_read_b128 v[164:167], v192 offset:17408
	v_exp_f32_e32 v209, v73
	v_add_f32_e32 v208, 1.0, v208
	v_mfma_f32_32x32x16_f16 v[96:111], a[20:23], v[168:171], v[96:111]
	ds_read_b128 v[168:171], v192 offset:18432
	v_exp_f32_e32 v210, v74
	v_add_f32_e32 v209, 1.0, v209
	v_mfma_f32_32x32x16_f16 v[112:127], a[20:23], v[172:175], v[112:127]
	ds_read_b128 v[172:175], v192 offset:19456
	global_load_lds_dwordx4 v192, s[44:45] offset:3072 sc1
	v_exp_f32_e32 v211, v75
	v_add_f32_e32 v210, 1.0, v210
	s_waitcnt lgkmcnt(2)
	v_mfma_f32_32x32x16_f16 v[96:111], a[24:27], v[176:179], v[96:111]
	ds_read_b128 v[176:179], v192 offset:20480
	v_exp_f32_e32 v212, v76
	v_add_f32_e32 v211, 1.0, v211
	v_mfma_f32_32x32x16_f16 v[112:127], a[24:27], v[180:183], v[112:127]
	ds_read_b128 v[180:183], v192 offset:21504
	v_exp_f32_e32 v213, v77
	v_add_f32_e32 v212, 1.0, v212
	v_mfma_f32_32x32x16_f16 v[96:111], a[28:31], v[184:187], v[96:111]
	ds_read_b128 v[184:187], v192 offset:22528
	v_exp_f32_e32 v214, v78
	v_add_f32_e32 v213, 1.0, v213
	v_mfma_f32_32x32x16_f16 v[112:127], a[28:31], v[188:191], v[112:127]
	ds_read_b128 v[188:191], v192 offset:23552
	s_mov_b32 m0, s57
	s_add_u32 s44, s34, 0x11000
	s_addc_u32 s45, s35, 0
	global_load_lds_dwordx4 v192, s[44:45] sc1
	v_exp_f32_e32 v215, v79
	v_add_f32_e32 v214, 1.0, v214
	v_mfma_f32_32x32x16_f16 v[96:111], a[32:35], v[160:163], v[96:111]
	ds_read_b128 v[160:163], v192 offset:24576
	v_add_f32_e32 v215, 1.0, v215
	v_rcp_f32_e32 v200, v200
	v_mfma_f32_32x32x16_f16 v[112:127], a[32:35], v[164:167], v[112:127]
	ds_read_b128 v[164:167], v192 offset:25600
	v_rcp_f32_e32 v201, v201
	s_waitcnt lgkmcnt(2)
	v_mfma_f32_32x32x16_f16 v[96:111], a[36:39], v[168:171], v[96:111]
	ds_read_b128 v[168:171], v192 offset:26624
	v_rcp_f32_e32 v202, v202
	v_mfma_f32_32x32x16_f16 v[112:127], a[36:39], v[172:175], v[112:127]
	ds_read_b128 v[172:175], v192 offset:27648
	global_load_lds_dwordx4 v192, s[44:45] offset:1024 sc1
	v_rcp_f32_e32 v203, v203
	v_mfma_f32_32x32x16_f16 v[96:111], a[40:43], v[176:179], v[96:111]
	ds_read_b128 v[176:179], v192 offset:28672
	v_rcp_f32_e32 v204, v204
	v_mfma_f32_32x32x16_f16 v[112:127], a[40:43], v[180:183], v[112:127]
	ds_read_b128 v[180:183], v192 offset:29696
	v_rcp_f32_e32 v205, v205
	v_mul_f32_e32 v204, v204, v144
	v_mfma_f32_32x32x16_f16 v[96:111], a[44:47], v[184:187], v[96:111]
	ds_read_b128 v[184:187], v192 offset:30720
	v_rcp_f32_e32 v206, v206
	v_mul_f32_e32 v205, v205, v145
	v_mfma_f32_32x32x16_f16 v[112:127], a[44:47], v[188:191], v[112:127]
	ds_read_b128 v[188:191], v192 offset:31744
	global_load_lds_dwordx4 v192, s[44:45] offset:2048 sc1
	v_rcp_f32_e32 v207, v207
	v_mul_f32_e32 v206, v206, v146
	s_waitcnt vmcnt(10)
	s_barrier
	s_waitcnt lgkmcnt(2)
	v_mfma_f32_32x32x16_f16 v[96:111], a[48:51], v[160:163], v[96:111]
	ds_read_b128 v[160:163], v192 offset:32768
	v_rcp_f32_e32 v208, v208
	v_mul_f32_e32 v207, v207, v147
	v_mfma_f32_32x32x16_f16 v[112:127], a[48:51], v[164:167], v[112:127]
	ds_read_b128 v[164:167], v192 offset:33792
	v_rcp_f32_e32 v209, v209
	v_fmamk_f32 v208, v208, 0xc0b8aa3b, v198
	v_mfma_f32_32x32x16_f16 v[96:111], a[52:55], v[168:171], v[96:111]
	ds_read_b128 v[168:171], v192 offset:34816
	v_rcp_f32_e32 v210, v210
	v_fmamk_f32 v209, v209, 0xc0b8aa3b, v198
	v_fma_f32 v144, v200, v208, v204
	v_mfma_f32_32x32x16_f16 v[112:127], a[52:55], v[172:175], v[112:127]
	ds_read_b128 v[172:175], v192 offset:35840
	global_load_lds_dwordx4 v192, s[44:45] offset:3072 sc1
	v_rcp_f32_e32 v211, v211
	v_fmamk_f32 v210, v210, 0xc0b8aa3b, v198
	v_fma_f32 v145, v201, v209, v205
	v_mfma_f32_32x32x16_f16 v[96:111], a[56:59], v[176:179], v[96:111]
	ds_read_b128 v[176:179], v192 offset:36864
	v_rcp_f32_e32 v212, v212
	v_fmamk_f32 v211, v211, 0xc0b8aa3b, v198
	v_fma_f32 v146, v202, v210, v206
	v_mfma_f32_32x32x16_f16 v[112:127], a[56:59], v[180:183], v[112:127]
	ds_read_b128 v[180:183], v192 offset:37888
	v_rcp_f32_e32 v213, v213
	v_fma_f32 v147, v203, v211, v207
	s_waitcnt lgkmcnt(2)
	v_mfma_f32_32x32x16_f16 v[96:111], a[60:63], v[184:187], v[96:111]
	ds_read_b128 v[184:187], v192 offset:38912
	v_rcp_f32_e32 v214, v214
	v_mfma_f32_32x32x16_f16 v[112:127], a[60:63], v[188:191], v[112:127]
	ds_read_b128 v[188:191], v192 offset:39936
	s_mov_b32 m0, s58
	s_add_u32 s44, s34, 0x18000
	s_addc_u32 s45, s35, 0
	global_load_lds_dwordx4 v192, s[44:45] sc1
	v_rcp_f32_e32 v215, v215
	v_mfma_f32_32x32x16_f16 v[96:111], a[64:67], v[160:163], v[96:111]
	ds_read_b128 v[160:163], v192 offset:40960
	v_exp_f32_e32 v200, v144
	v_mfma_f32_32x32x16_f16 v[112:127], a[64:67], v[164:167], v[112:127]
	ds_read_b128 v[164:167], v192 offset:41984
	v_exp_f32_e32 v201, v145
	v_add_f32_e32 v200, 1.0, v200
	v_mfma_f32_32x32x16_f16 v[96:111], a[68:71], v[168:171], v[96:111]
	ds_read_b128 v[168:171], v192 offset:43008
	v_exp_f32_e32 v202, v146
	v_add_f32_e32 v201, 1.0, v201
	v_mfma_f32_32x32x16_f16 v[112:127], a[68:71], v[172:175], v[112:127]
	ds_read_b128 v[172:175], v192 offset:44032
	global_load_lds_dwordx4 v192, s[44:45] offset:1024 sc1
	v_exp_f32_e32 v203, v147
	v_add_f32_e32 v202, 1.0, v202
	s_waitcnt lgkmcnt(2)
	v_mfma_f32_32x32x16_f16 v[96:111], a[72:75], v[176:179], v[96:111]
	ds_read_b128 v[176:179], v192 offset:45056
	v_add_f32_e32 v203, 1.0, v203
	v_rcp_f32_e32 v200, v200
	v_mfma_f32_32x32x16_f16 v[112:127], a[72:75], v[180:183], v[112:127]
	ds_read_b128 v[180:183], v192 offset:46080
	v_rcp_f32_e32 v201, v201
	v_fma_f32 v200, v200, 2.0, -1.0
	v_mfma_f32_32x32x16_f16 v[96:111], a[76:79], v[184:187], v[96:111]
	ds_read_b128 v[184:187], v192 offset:47104
	v_rcp_f32_e32 v202, v202
	v_fma_f32 v201, v201, 2.0, -1.0
	v_mul_f32_e32 v216, v212, v200
	v_mfma_f32_32x32x16_f16 v[112:127], a[76:79], v[188:191], v[112:127]
	ds_read_b128 v[188:191], v192 offset:48128
	global_load_lds_dwordx4 v192, s[44:45] offset:2048 sc1
	v_rcp_f32_e32 v203, v203
	v_fma_f32 v202, v202, 2.0, -1.0
	v_mul_f32_e32 v217, v213, v201
	v_mfma_f32_32x32x16_f16 v[96:111], a[80:83], v[160:163], v[96:111]
	ds_read_b128 v[160:163], v192 offset:49152
	v_fma_f32 v203, v203, 2.0, -1.0
	v_mul_f32_e32 v218, v214, v202
	v_exp_f32_e32 v200, v80
	v_mfma_f32_32x32x16_f16 v[112:127], a[80:83], v[164:167], v[112:127]
	ds_read_b128 v[164:167], v192 offset:50176
	v_mul_f32_e32 v219, v215, v203
	v_cvt_pk_f16_f32 v220, v216, v217
	v_exp_f32_e32 v201, v81
	s_waitcnt lgkmcnt(2)
	v_mfma_f32_32x32x16_f16 v[96:111], a[84:87], v[168:171], v[96:111]
	ds_read_b128 v[168:171], v192 offset:51200
	v_cvt_pk_f16_f32 v221, v218, v219
	v_exp_f32_e32 v202, v82
	v_add_f32_e32 v200, 1.0, v200
	v_mfma_f32_32x32x16_f16 v[112:127], a[84:87], v[172:175], v[112:127]
	ds_read_b128 v[172:175], v192 offset:52224
	global_load_lds_dwordx4 v192, s[44:45] offset:3072 sc1
	s_cmp_eq_u32 s33, s60
	s_cbranch_scc1 .LE_ht42

.LE_join49:
	v_mfma_f32_32x32x16_f16 v[112:127], a[168:171], v[180:183], v[112:127]
	ds_read_b128 v[180:183], v193 offset:29696
	v_mfma_f32_32x32x16_f16 v[96:111], a[172:175], v[184:187], v[96:111]
	ds_read_b128 v[184:187], v193 offset:30720
	v_mfma_f32_32x32x16_f16 v[112:127], a[172:175], v[188:191], v[112:127]
	ds_read_b128 v[188:191], v193 offset:31744
	global_load_lds_dwordx4 v192, s[44:45] offset:2048 sc1
	s_waitcnt vmcnt(8)
	s_barrier
	v_mfma_f32_32x32x16_f16 v[96:111], a[176:179], v[160:163], v[96:111]
	ds_read_b128 v[160:163], v193 offset:32768
	v_mfma_f32_32x32x16_f16 v[112:127], a[176:179], v[164:167], v[112:127]
	ds_read_b128 v[164:167], v193 offset:33792
	s_waitcnt lgkmcnt(2)
	v_mfma_f32_32x32x16_f16 v[96:111], a[180:183], v[168:171], v[96:111]
	ds_read_b128 v[168:171], v193 offset:34816
	v_mfma_f32_32x32x16_f16 v[112:127], a[180:183], v[172:175], v[112:127]
	ds_read_b128 v[172:175], v193 offset:35840
	global_load_lds_dwordx4 v192, s[44:45] offset:3072 sc1
	v_mfma_f32_32x32x16_f16 v[96:111], a[184:187], v[176:179], v[96:111]
	ds_read_b128 v[176:179], v193 offset:36864
	v_mfma_f32_32x32x16_f16 v[112:127], a[184:187], v[180:183], v[112:127]
	ds_read_b128 v[180:183], v193 offset:37888
	v_mfma_f32_32x32x16_f16 v[96:111], a[188:191], v[184:187], v[96:111]
	ds_read_b128 v[184:187], v193 offset:38912
	v_mfma_f32_32x32x16_f16 v[112:127], a[188:191], v[188:191], v[112:127]
	ds_read_b128 v[188:191], v193 offset:39936
	s_mov_b32 m0, s54
	s_add_u32 s44, s34, 0x8000
	s_addc_u32 s45, s35, 0
	global_load_lds_dwordx4 v192, s[44:45] sc1
	s_waitcnt lgkmcnt(2)
	v_mfma_f32_32x32x16_f16 v[96:111], a[192:195], v[160:163], v[96:111]
	ds_read_b128 v[160:163], v193 offset:40960
	v_mfma_f32_32x32x16_f16 v[112:127], a[192:195], v[164:167], v[112:127]
	ds_read_b128 v[164:167], v193 offset:41984
	v_mfma_f32_32x32x16_f16 v[96:111], a[196:199], v[168:171], v[96:111]
	ds_read_b128 v[168:171], v193 offset:43008
	v_mfma_f32_32x32x16_f16 v[112:127], a[196:199], v[172:175], v[112:127]
	ds_read_b128 v[172:175], v193 offset:44032
	global_load_lds_dwordx4 v192, s[44:45] offset:1024 sc1
	v_mfma_f32_32x32x16_f16 v[96:111], a[200:203], v[176:179], v[96:111]
	ds_read_b128 v[176:179], v193 offset:45056
	v_mfma_f32_32x32x16_f16 v[112:127], a[200:203], v[180:183], v[112:127]
	ds_read_b128 v[180:183], v193 offset:46080
	s_waitcnt lgkmcnt(2)
	v_mfma_f32_32x32x16_f16 v[96:111], a[204:207], v[184:187], v[96:111]
	ds_read_b128 v[184:187], v193 offset:47104
	v_mfma_f32_32x32x16_f16 v[112:127], a[204:207], v[188:191], v[112:127]
	ds_read_b128 v[188:191], v193 offset:48128
	global_load_lds_dwordx4 v192, s[44:45] offset:2048 sc1
	v_mfma_f32_32x32x16_f16 v[96:111], a[208:211], v[160:163], v[96:111]
	ds_read_b128 v[160:163], v193 offset:49152
	v_mfma_f32_32x32x16_f16 v[112:127], a[208:211], v[164:167], v[112:127]
	ds_read_b128 v[164:167], v193 offset:50176
	s_waitcnt vmcnt(5)
	s_barrier
	v_mov_b32_e32 v199, 3
	s_cmp_eq_u32 s31, 0
	s_cbranch_scc1 .LE_slow50
	global_store_dword v197, v199, s[40:41]
.LE_join51:
	v_mfma_f32_32x32x16_f16 v[96:111], a[212:215], v[168:171], v[96:111]
	ds_read_b128 v[168:171], v193 offset:51200
	v_mfma_f32_32x32x16_f16 v[112:127], a[212:215], v[172:175], v[112:127]
	ds_read_b128 v[172:175], v193 offset:52224
	global_load_lds_dwordx4 v192, s[44:45] offset:3072 sc1
	s_waitcnt lgkmcnt(2)
	v_mfma_f32_32x32x16_f16 v[96:111], a[216:219], v[176:179], v[96:111]
	ds_read_b128 v[176:179], v193 offset:53248
	v_mfma_f32_32x32x16_f16 v[112:127], a[216:219], v[180:183], v[112:127]
	ds_read_b128 v[180:183], v193 offset:54272
	v_mfma_f32_32x32x16_f16 v[96:111], a[220:223], v[184:187], v[96:111]
	ds_read_b128 v[184:187], v193 offset:55296
	v_mfma_f32_32x32x16_f16 v[112:127], a[220:223], v[188:191], v[112:127]
	ds_read_b128 v[188:191], v193 offset:56320
	s_mov_b32 m0, s55
	s_add_u32 s44, s34, 0x9000
	s_addc_u32 s45, s35, 0
	global_load_lds_dwordx4 v192, s[44:45] sc1
	v_mfma_f32_32x32x16_f16 v[96:111], a[224:227], v[160:163], v[96:111]
	ds_read_b128 v[160:163], v193 offset:57344
	v_mfma_f32_32x32x16_f16 v[112:127], a[224:227], v[164:167], v[112:127]
	ds_read_b128 v[164:167], v193 offset:58368
	s_waitcnt lgkmcnt(2)
	v_mfma_f32_32x32x16_f16 v[96:111], a[228:231], v[168:171], v[96:111]
	ds_read_b128 v[168:171], v193 offset:59392
	v_mfma_f32_32x32x16_f16 v[112:127], a[228:231], v[172:175], v[112:127]
	ds_read_b128 v[172:175], v193 offset:60416
	global_load_lds_dwordx4 v192, s[44:45] offset:1024 sc1
	v_mfma_f32_32x32x16_f16 v[96:111], a[232:235], v[176:179], v[96:111]
	ds_read_b128 v[176:179], v193 offset:61440
	v_mfma_f32_32x32x16_f16 v[112:127], a[232:235], v[180:183], v[112:127]
	ds_read_b128 v[180:183], v193 offset:62464
	v_mfma_f32_32x32x16_f16 v[96:111], a[236:239], v[184:187], v[96:111]
	ds_read_b128 v[184:187], v193 offset:63488
	v_mfma_f32_32x32x16_f16 v[112:127], a[236:239], v[188:191], v[112:127]
	ds_read_b128 v[188:191], v193 offset:64512
	global_load_lds_dwordx4 v192, s[44:45] offset:2048 sc1
	s_waitcnt vmcnt(8)
	s_barrier
	s_waitcnt lgkmcnt(2)
	v_mfma_f32_32x32x16_f16 v[96:111], a[240:243], v[160:163], v[96:111]
	ds_read_b128 v[160:163], v192 offset:0
	v_mfma_f32_32x32x16_f16 v[112:127], a[240:243], v[164:167], v[112:127]
	ds_read_b128 v[164:167], v192 offset:1024
	v_mfma_f32_32x32x16_f16 v[96:111], a[244:247], v[168:171], v[96:111]
	ds_read_b128 v[168:171], v192 offset:2048
	v_mfma_f32_32x32x16_f16 v[112:127], a[244:247], v[172:175], v[112:127]
	ds_read_b128 v[172:175], v192 offset:3072
	global_load_lds_dwordx4 v192, s[44:45] offset:3072 sc1
	v_mfma_f32_32x32x16_f16 v[96:111], a[248:251], v[176:179], v[96:111]
	ds_read_b128 v[176:179], v192 offset:4096
	v_mfma_f32_32x32x16_f16 v[112:127], a[248:251], v[180:183], v[112:127]
	ds_read_b128 v[180:183], v192 offset:5120
	s_waitcnt lgkmcnt(2)
	v_mfma_f32_32x32x16_f16 v[96:111], a[252:255], v[184:187], v[96:111]
	ds_read_b128 v[184:187], v192 offset:6144
	v_mfma_f32_32x32x16_f16 v[112:127], a[252:255], v[188:191], v[112:127]
	ds_read_b128 v[188:191], v192 offset:7168
	s_mov_b32 m0, s56
	s_add_u32 s44, s34, 0x10000
	s_addc_u32 s45, s35, 0
	global_load_lds_dwordx4 v192, s[44:45] sc1
	s_add_u32 s33, s33, 1
	s_cmp_lt_u32 s33, s28
	s_cbranch_scc1 .LE_loop12

.LD_join19:
	s_waitcnt lgkmcnt(3)
	v_mfma_f32_32x32x16_f16 v[0:15], a[180:183], v[168:171], v[0:15]
	ds_read_b128 v[168:171], v193 offset:34816
	v_mfma_f32_32x32x16_f16 v[16:31], a[180:183], v[172:175], v[16:31]
	ds_read_b128 v[172:175], v193 offset:35840
	global_load_lds_dwordx4 v192, s[44:45] offset:3072 sc1
	v_mfma_f32_32x32x16_f16 v[0:15], a[184:187], v[176:179], v[0:15]
	ds_read_b128 v[176:179], v193 offset:36864
	v_mfma_f32_32x32x16_f16 v[16:31], a[184:187], v[180:183], v[16:31]
	ds_read_b128 v[180:183], v193 offset:37888
	v_mfma_f32_32x32x16_f16 v[0:15], a[188:191], v[184:187], v[0:15]
	ds_read_b128 v[184:187], v193 offset:38912
	v_mfma_f32_32x32x16_f16 v[16:31], a[188:191], v[188:191], v[16:31]
	ds_read_b128 v[188:191], v193 offset:39936
	s_mov_b32 m0, s54
	s_add_u32 s44, s34, 0x8000
	s_addc_u32 s45, s35, 0
	global_load_lds_dwordx4 v192, s[44:45] sc1
	s_waitcnt lgkmcnt(2)
	v_mfma_f32_32x32x16_f16 v[0:15], a[192:195], v[160:163], v[0:15]
	ds_read_b128 v[160:163], v193 offset:40960
	v_mfma_f32_32x32x16_f16 v[16:31], a[192:195], v[164:167], v[16:31]
	ds_read_b128 v[164:167], v193 offset:41984
	v_mfma_f32_32x32x16_f16 v[0:15], a[196:199], v[168:171], v[0:15]
	ds_read_b128 v[168:171], v193 offset:43008
	v_mfma_f32_32x32x16_f16 v[16:31], a[196:199], v[172:175], v[16:31]
	ds_read_b128 v[172:175], v193 offset:44032
	global_load_lds_dwordx4 v192, s[44:45] offset:1024 sc1
	v_mfma_f32_32x32x16_f16 v[0:15], a[200:203], v[176:179], v[0:15]
	ds_read_b128 v[176:179], v193 offset:45056
	v_mfma_f32_32x32x16_f16 v[16:31], a[200:203], v[180:183], v[16:31]
	ds_read_b128 v[180:183], v193 offset:46080
	s_waitcnt lgkmcnt(2)
	v_mfma_f32_32x32x16_f16 v[0:15], a[204:207], v[184:187], v[0:15]
	ds_read_b128 v[184:187], v193 offset:47104
	v_mfma_f32_32x32x16_f16 v[16:31], a[204:207], v[188:191], v[16:31]
	ds_read_b128 v[188:191], v193 offset:48128
	global_load_lds_dwordx4 v192, s[44:45] offset:2048 sc1
	v_mfma_f32_32x32x16_f16 v[0:15], a[208:211], v[160:163], v[0:15]
	ds_read_b128 v[160:163], v193 offset:49152
	v_mfma_f32_32x32x16_f16 v[16:31], a[208:211], v[164:167], v[16:31]
	ds_read_b128 v[164:167], v193 offset:50176
	v_mfma_f32_32x32x16_f16 v[0:15], a[212:215], v[168:171], v[0:15]
	ds_read_b128 v[168:171], v193 offset:51200
	v_mfma_f32_32x32x16_f16 v[16:31], a[212:215], v[172:175], v[16:31]
	ds_read_b128 v[172:175], v193 offset:52224
	global_load_lds_dwordx4 v192, s[44:45] offset:3072 sc1
	s_waitcnt lgkmcnt(2)
	v_mfma_f32_32x32x16_f16 v[0:15], a[216:219], v[176:179], v[0:15]
	ds_read_b128 v[176:179], v193 offset:53248
	v_mfma_f32_32x32x16_f16 v[16:31], a[216:219], v[180:183], v[16:31]
	ds_read_b128 v[180:183], v193 offset:54272
	v_mfma_f32_32x32x16_f16 v[0:15], a[220:223], v[184:187], v[0:15]
	ds_read_b128 v[184:187], v193 offset:55296
	s_waitcnt vmcnt(5)
	s_barrier
	v_mov_b32_e32 v199, 4
	s_cmp_eq_u32 s31, 0
	s_cbranch_scc1 .LD_slow20
	global_store_dword v197, v199, s[40:41]
.LD_join21:
	ds_read_b64 v[200:201], v249 offset:1536
	ds_read_b64 v[202:203], v249 offset:3584
	ds_read_b64 v[204:205], v249 offset:5632
	ds_read_b64 v[206:207], v249 offset:7680
	v_mfma_f32_32x32x16_f16 v[16:31], a[220:223], v[188:191], v[16:31]
	ds_read_b128 v[188:191], v193 offset:56320
	s_mov_b32 m0, s55
	s_add_u32 s44, s34, 0x9000
	s_addc_u32 s45, s35, 0
	global_load_lds_dwordx4 v192, s[44:45] sc1
	v_mfma_f32_32x32x16_f16 v[0:15], a[224:227], v[160:163], v[0:15]
	ds_read_b128 v[160:163], v193 offset:57344
	v_mfma_f32_32x32x16_f16 v[16:31], a[224:227], v[164:167], v[16:31]
	ds_read_b128 v[164:167], v193 offset:58368
	s_waitcnt lgkmcnt(2)
	v_mfma_f32_32x32x16_f16 v[0:15], a[228:231], v[168:171], v[0:15]
	ds_read_b128 v[168:171], v193 offset:59392
	v_mfma_f32_32x32x16_f16 v[16:31], a[228:231], v[172:175], v[16:31]
	ds_read_b128 v[172:175], v193 offset:60416
	global_load_lds_dwordx4 v192, s[44:45] offset:1024 sc1
	v_mfma_f32_32x32x16_f16 v[0:15], a[232:235], v[176:179], v[0:15]
	ds_read_b128 v[176:179], v193 offset:61440
	v_mfma_f32_32x32x16_f16 v[16:31], a[232:235], v[180:183], v[16:31]
	ds_read_b128 v[180:183], v193 offset:62464
	v_mfma_f32_32x32x16_f16 v[0:15], a[236:239], v[184:187], v[0:15]
	ds_read_b128 v[184:187], v193 offset:63488
	v_mfma_f32_32x32x16_f16 v[16:31], a[236:239], v[188:191], v[16:31]
	ds_read_b128 v[188:191], v193 offset:64512
	global_load_lds_dwordx4 v192, s[44:45] offset:2048 sc1
	s_waitcnt vmcnt(8)
	s_barrier
	s_waitcnt lgkmcnt(2)
	v_mfma_f32_32x32x16_f16 v[0:15], a[240:243], v[160:163], v[0:15]
	ds_read_b128 v[160:163], v192 offset:0
	v_mfma_f32_32x32x16_f16 v[16:31], a[240:243], v[164:167], v[16:31]
	ds_read_b128 v[164:167], v192 offset:1024
	v_mfma_f32_32x32x16_f16 v[0:15], a[244:247], v[168:171], v[0:15]
	ds_read_b128 v[168:171], v192 offset:2048
	v_add_f32_e32 v200, v200, v202
	v_add_f32_e32 v201, v201, v203
	v_add_f32_e32 v200, v200, v204
	v_add_f32_e32 v201, v201, v205
	v_add_f32_e32 v200, v200, v206
	v_add_f32_e32 v201, v201, v207
	global_store_dwordx2 v250, v[200:201], s[72:73]
	v_mfma_f32_32x32x16_f16 v[16:31], a[244:247], v[172:175], v[16:31]
	ds_read_b128 v[172:175], v192 offset:3072
	global_load_lds_dwordx4 v192, s[44:45] offset:3072 sc1
	v_mfma_f32_32x32x16_f16 v[0:15], a[248:251], v[176:179], v[0:15]
	ds_read_b128 v[176:179], v192 offset:4096
	v_mfma_f32_32x32x16_f16 v[16:31], a[248:251], v[180:183], v[16:31]
	ds_read_b128 v[180:183], v192 offset:5120
	s_waitcnt lgkmcnt(2)
	v_mfma_f32_32x32x16_f16 v[0:15], a[252:255], v[184:187], v[0:15]
	ds_read_b128 v[184:187], v192 offset:6144
	s_and_b32 s64, s33, 1
	s_lshl_b32 s64, s64, 22
	s_add_u32 s64, s64, s50
	s_add_u32 s36, s6, s64
	s_addc_u32 s37, s7, 0
	s_lshl_b32 s64, s33, 3
	s_add_u32 s64, s64, s29
	s_lshl_b32 s64, s64, 5
	s_add_u32 s64, s64, s30
	s_lshl_b32 s64, s64, 2
	s_add_u32 s40, s8, s64
	s_addc_u32 s41, s9, 0
	s_lshl_b32 s64, s33, 19
	s_add_u32 s72, s62, s64
	s_addc_u32 s73, s63, 0
	v_mfma_f32_32x32x16_f16 v[16:31], a[252:255], v[188:191], v[16:31]
	ds_read_b128 v[188:191], v192 offset:7168
	s_mov_b32 m0, s56
	s_add_u32 s44, s34, 0x10000
	s_addc_u32 s45, s35, 0
	global_load_lds_dwordx4 v192, s[44:45] sc1
	s_nop 3
	s_waitcnt lgkmcnt(2)
	v_mfma_f32_32x32x16_f16 v[32:47], a[0:3], v[160:163], v[32:47]
	ds_read_b128 v[160:163], v192 offset:8192
	v_exp_f32_e32 v200, v0
	v_mfma_f32_32x32x16_f16 v[48:63], a[0:3], v[164:167], v[48:63]
	ds_read_b128 v[164:167], v192 offset:9216
	s_lshl_b32 s64, s71, 3
	s_add_u32 s64, s64, s29
	s_lshl_b32 s64, s64, 7
	s_add_u32 s38, s8, s64
	s_addc_u32 s39, s9, 0
	global_load_dword v251, v196, s[38:39] sc1
	v_exp_f32_e32 v201, v1
	v_add_f32_e32 v200, 1.0, v200
	v_mfma_f32_32x32x16_f16 v[32:47], a[4:7], v[168:171], v[32:47]
	ds_read_b128 v[168:171], v192 offset:10240
	v_exp_f32_e32 v202, v2
	v_add_f32_e32 v201, 1.0, v201
	v_mfma_f32_32x32x16_f16 v[48:63], a[4:7], v[172:175], v[48:63]
	ds_read_b128 v[172:175], v192 offset:11264
	global_load_lds_dwordx4 v192, s[44:45] offset:1024 sc1
	v_exp_f32_e32 v203, v3
	v_add_f32_e32 v202, 1.0, v202
	v_mfma_f32_32x32x16_f16 v[32:47], a[8:11], v[176:179], v[32:47]
	ds_read_b128 v[176:179], v192 offset:12288
	v_exp_f32_e32 v204, v4
	v_add_f32_e32 v203, 1.0, v203
	v_mfma_f32_32x32x16_f16 v[48:63], a[8:11], v[180:183], v[48:63]
	ds_read_b128 v[180:183], v192 offset:13312
	v_exp_f32_e32 v205, v5
	v_add_f32_e32 v204, 1.0, v204
	s_waitcnt lgkmcnt(2)
	v_mfma_f32_32x32x16_f16 v[32:47], a[12:15], v[184:187], v[32:47]
	ds_read_b128 v[184:187], v192 offset:14336
	v_exp_f32_e32 v206, v6
	v_add_f32_e32 v205, 1.0, v205
	v_mfma_f32_32x32x16_f16 v[48:63], a[12:15], v[188:191], v[48:63]
	ds_read_b128 v[188:191], v192 offset:15360
	global_load_lds_dwordx4 v192, s[44:45] offset:2048 sc1
	v_exp_f32_e32 v207, v7
	v_add_f32_e32 v206, 1.0, v206
	v_mfma_f32_32x32x16_f16 v[32:47], a[16:19], v[160:163], v[32:47]
	ds_read_b128 v[160:163], v192 offset:16384
	v_exp_f32_e32 v208, v8
	v_add_f32_e32 v207, 1.0, v207
	v_mfma_f32_32x32x16_f16 v[48:63], a[16:19], v[164:167], v[48:63]
	ds_read_b128 v[164:167], v192 offset:17408
	v_exp_f32_e32 v209, v9
	v_add_f32_e32 v208, 1.0, v208
	v_mfma_f32_32x32x16_f16 v[32:47], a[20:23], v[168:171], v[32:47]
	ds_read_b128 v[168:171], v192 offset:18432
	v_exp_f32_e32 v210, v10
	v_add_f32_e32 v209, 1.0, v209
	v_mfma_f32_32x32x16_f16 v[48:63], a[20:23], v[172:175], v[48:63]
	ds_read_b128 v[172:175], v192 offset:19456
	global_load_lds_dwordx4 v192, s[44:45] offset:3072 sc1
	v_exp_f32_e32 v211, v11
	v_add_f32_e32 v210, 1.0, v210
	s_waitcnt lgkmcnt(2)
	v_mfma_f32_32x32x16_f16 v[32:47], a[24:27], v[176:179], v[32:47]
	ds_read_b128 v[176:179], v192 offset:20480
	v_exp_f32_e32 v212, v12
	v_add_f32_e32 v211, 1.0, v211
	v_mfma_f32_32x32x16_f16 v[48:63], a[24:27], v[180:183], v[48:63]
	ds_read_b128 v[180:183], v192 offset:21504
	v_exp_f32_e32 v213, v13
	v_add_f32_e32 v212, 1.0, v212
	v_mfma_f32_32x32x16_f16 v[32:47], a[28:31], v[184:187], v[32:47]
	ds_read_b128 v[184:187], v192 offset:22528
	v_exp_f32_e32 v214, v14
	v_add_f32_e32 v213, 1.0, v213
	v_mfma_f32_32x32x16_f16 v[48:63], a[28:31], v[188:191], v[48:63]
	ds_read_b128 v[188:191], v192 offset:23552
	s_mov_b32 m0, s57
	s_add_u32 s44, s34, 0x11000
	s_addc_u32 s45, s35, 0
	global_load_lds_dwordx4 v192, s[44:45] sc1
	v_exp_f32_e32 v215, v15
	v_add_f32_e32 v214, 1.0, v214
	v_mfma_f32_32x32x16_f16 v[32:47], a[32:35], v[160:163], v[32:47]
	ds_read_b128 v[160:163], v192 offset:24576
	v_add_f32_e32 v215, 1.0, v215
	v_rcp_f32_e32 v200, v200
	v_mfma_f32_32x32x16_f16 v[48:63], a[32:35], v[164:167], v[48:63]
	ds_read_b128 v[164:167], v192 offset:25600
	v_rcp_f32_e32 v201, v201
	s_waitcnt lgkmcnt(2)
	v_mfma_f32_32x32x16_f16 v[32:47], a[36:39], v[168:171], v[32:47]
	ds_read_b128 v[168:171], v192 offset:26624
	v_rcp_f32_e32 v202, v202
	v_mfma_f32_32x32x16_f16 v[48:63], a[36:39], v[172:175], v[48:63]
	ds_read_b128 v[172:175], v192 offset:27648
	global_load_lds_dwordx4 v192, s[44:45] offset:1024 sc1
	v_rcp_f32_e32 v203, v203
	v_mfma_f32_32x32x16_f16 v[32:47], a[40:43], v[176:179], v[32:47]
	ds_read_b128 v[176:179], v192 offset:28672
	v_rcp_f32_e32 v204, v204
	v_mfma_f32_32x32x16_f16 v[48:63], a[40:43], v[180:183], v[48:63]
	ds_read_b128 v[180:183], v192 offset:29696
	v_rcp_f32_e32 v205, v205
	v_mul_f32_e32 v204, v204, v128
	v_mfma_f32_32x32x16_f16 v[32:47], a[44:47], v[184:187], v[32:47]
	ds_read_b128 v[184:187], v192 offset:30720
	v_rcp_f32_e32 v206, v206
	v_mul_f32_e32 v205, v205, v129
	v_mfma_f32_32x32x16_f16 v[48:63], a[44:47], v[188:191], v[48:63]
	ds_read_b128 v[188:191], v192 offset:31744
	global_load_lds_dwordx4 v192, s[44:45] offset:2048 sc1
	v_rcp_f32_e32 v207, v207
	v_mul_f32_e32 v206, v206, v130
	s_waitcnt vmcnt(8)
	s_barrier
	s_waitcnt lgkmcnt(2)
	v_mfma_f32_32x32x16_f16 v[32:47], a[48:51], v[160:163], v[32:47]
	ds_read_b128 v[160:163], v192 offset:32768
	v_rcp_f32_e32 v208, v208
	v_mul_f32_e32 v207, v207, v131
	v_mfma_f32_32x32x16_f16 v[48:63], a[48:51], v[164:167], v[48:63]
	ds_read_b128 v[164:167], v192 offset:33792
	v_rcp_f32_e32 v209, v209
	v_fmamk_f32 v208, v208, 0xc0b8aa3b, v198
	v_mfma_f32_32x32x16_f16 v[32:47], a[52:55], v[168:171], v[32:47]
	ds_read_b128 v[168:171], v192 offset:34816
	v_rcp_f32_e32 v210, v210
	v_fmamk_f32 v209, v209, 0xc0b8aa3b, v198
	v_fma_f32 v128, v200, v208, v204
	v_mfma_f32_32x32x16_f16 v[48:63], a[52:55], v[172:175], v[48:63]
	ds_read_b128 v[172:175], v192 offset:35840
	global_load_lds_dwordx4 v192, s[44:45] offset:3072 sc1
	v_rcp_f32_e32 v211, v211
	v_fmamk_f32 v210, v210, 0xc0b8aa3b, v198
	v_fma_f32 v129, v201, v209, v205
	v_mfma_f32_32x32x16_f16 v[32:47], a[56:59], v[176:179], v[32:47]
	ds_read_b128 v[176:179], v192 offset:36864
	v_rcp_f32_e32 v212, v212
	v_fmamk_f32 v211, v211, 0xc0b8aa3b, v198
	v_fma_f32 v130, v202, v210, v206
	v_mfma_f32_32x32x16_f16 v[48:63], a[56:59], v[180:183], v[48:63]
	ds_read_b128 v[180:183], v192 offset:37888
	v_rcp_f32_e32 v213, v213
	v_fma_f32 v131, v203, v211, v207
	s_waitcnt lgkmcnt(2)
	v_mfma_f32_32x32x16_f16 v[32:47], a[60:63], v[184:187], v[32:47]
	ds_read_b128 v[184:187], v192 offset:38912
	v_rcp_f32_e32 v214, v214
	v_mfma_f32_32x32x16_f16 v[48:63], a[60:63], v[188:191], v[48:63]
	ds_read_b128 v[188:191], v192 offset:39936
	s_mov_b32 m0, s58
	s_add_u32 s44, s34, 0x18000
	s_addc_u32 s45, s35, 0
	global_load_lds_dwordx4 v192, s[44:45] sc1
	v_rcp_f32_e32 v215, v215
	v_mfma_f32_32x32x16_f16 v[32:47], a[64:67], v[160:163], v[32:47]
	ds_read_b128 v[160:163], v192 offset:40960
	v_exp_f32_e32 v200, v128
	v_mfma_f32_32x32x16_f16 v[48:63], a[64:67], v[164:167], v[48:63]
	ds_read_b128 v[164:167], v192 offset:41984
	v_exp_f32_e32 v201, v129
	v_add_f32_e32 v200, 1.0, v200
	v_mfma_f32_32x32x16_f16 v[32:47], a[68:71], v[168:171], v[32:47]
	ds_read_b128 v[168:171], v192 offset:43008
	v_exp_f32_e32 v202, v130
	v_add_f32_e32 v201, 1.0, v201
	v_mfma_f32_32x32x16_f16 v[48:63], a[68:71], v[172:175], v[48:63]
	ds_read_b128 v[172:175], v192 offset:44032
	global_load_lds_dwordx4 v192, s[44:45] offset:1024 sc1
	v_exp_f32_e32 v203, v131
	v_add_f32_e32 v202, 1.0, v202
	s_waitcnt lgkmcnt(2)
	v_mfma_f32_32x32x16_f16 v[32:47], a[72:75], v[176:179], v[32:47]
	ds_read_b128 v[176:179], v192 offset:45056
	v_add_f32_e32 v203, 1.0, v203
	v_rcp_f32_e32 v200, v200
	v_mfma_f32_32x32x16_f16 v[48:63], a[72:75], v[180:183], v[48:63]
	ds_read_b128 v[180:183], v192 offset:46080
	v_rcp_f32_e32 v201, v201
	v_fma_f32 v200, v200, 2.0, -1.0
	v_mfma_f32_32x32x16_f16 v[32:47], a[76:79], v[184:187], v[32:47]
	ds_read_b128 v[184:187], v192 offset:47104
	v_rcp_f32_e32 v202, v202
	v_fma_f32 v201, v201, 2.0, -1.0
	v_mul_f32_e32 v216, v212, v200
	v_mfma_f32_32x32x16_f16 v[48:63], a[76:79], v[188:191], v[48:63]
	ds_read_b128 v[188:191], v192 offset:48128
	global_load_lds_dwordx4 v192, s[44:45] offset:2048 sc1
	v_rcp_f32_e32 v203, v203
	v_fma_f32 v202, v202, 2.0, -1.0
	v_mul_f32_e32 v217, v213, v201
	v_mfma_f32_32x32x16_f16 v[32:47], a[80:83], v[160:163], v[32:47]
	ds_read_b128 v[160:163], v192 offset:49152
	v_fma_f32 v203, v203, 2.0, -1.0
	v_mul_f32_e32 v218, v214, v202
	v_exp_f32_e32 v200, v16
	v_mfma_f32_32x32x16_f16 v[48:63], a[80:83], v[164:167], v[48:63]
	ds_read_b128 v[164:167], v192 offset:50176
	v_mul_f32_e32 v219, v215, v203
	v_mul_f32_e32 v236, v216, v228
	v_exp_f32_e32 v201, v17
	s_waitcnt lgkmcnt(2)
	v_mfma_f32_32x32x16_f16 v[32:47], a[84:87], v[168:171], v[32:47]
	ds_read_b128 v[168:171], v192 offset:51200
	v_mul_f32_e32 v237, v216, v232
	v_fmac_f32_e32 v236, v217, v229
	v_exp_f32_e32 v202, v18
	v_mfma_f32_32x32x16_f16 v[48:63], a[84:87], v[172:175], v[48:63]
	ds_read_b128 v[172:175], v192 offset:52224
	global_load_lds_dwordx4 v192, s[44:45] offset:3072 sc1
	v_fmac_f32_e32 v237, v217, v233
	v_fmac_f32_e32 v236, v218, v230
	v_exp_f32_e32 v203, v19
	v_mfma_f32_32x32x16_f16 v[32:47], a[88:91], v[176:179], v[32:47]
	ds_read_b128 v[176:179], v192 offset:53248
	v_fmac_f32_e32 v237, v218, v234
	v_fmac_f32_e32 v236, v219, v231
	v_exp_f32_e32 v204, v20
	v_mfma_f32_32x32x16_f16 v[48:63], a[88:91], v[180:183], v[48:63]
	ds_read_b128 v[180:183], v192 offset:54272
	v_fmac_f32_e32 v237, v219, v235
	v_mov_b32_e32 v238, v236
	v_exp_f32_e32 v205, v21
	v_mfma_f32_32x32x16_f16 v[32:47], a[92:95], v[184:187], v[32:47]
	ds_read_b128 v[184:187], v192 offset:55296
	v_mov_b32_e32 v240, v237
	v_cvt_pk_f16_f32 v220, v216, v217
	v_exp_f32_e32 v206, v22
	v_mfma_f32_32x32x16_f16 v[48:63], a[92:95], v[188:191], v[48:63]
	ds_read_b128 v[188:191], v192 offset:56320
	s_mov_b32 m0, s59
	s_add_u32 s44, s34, 0x19000
	s_addc_u32 s45, s35, 0
	global_load_lds_dwordx4 v192, s[44:45] sc1
	v_permlane32_swap_b32_e32 v236, v238
	v_permlane32_swap_b32_e32 v237, v240
	v_add_f32_e32 v238, v236, v238
	v_add_f32_e32 v239, v237, v240
	ds_write_b64 v248, v[238:239] offset:0
	v_exp_f32_e32 v207, v23
	s_waitcnt lgkmcnt(3)
	v_mfma_f32_32x32x16_f16 v[32:47], a[96:99], v[160:163], v[32:47]
	ds_read_b128 v[160:163], v192 offset:57344
	v_cvt_pk_f16_f32 v221, v218, v219
	v_exp_f32_e32 v208, v24
	v_add_f32_e32 v200, 1.0, v200
	v_mfma_f32_32x32x16_f16 v[48:63], a[96:99], v[164:167], v[48:63]
	ds_read_b128 v[164:167], v192 offset:58368
	v_exp_f32_e32 v209, v25
	v_add_f32_e32 v201, 1.0, v201
	v_add_f32_e32 v202, 1.0, v202
	v_mfma_f32_32x32x16_f16 v[32:47], a[100:103], v[168:171], v[32:47]
	ds_read_b128 v[168:171], v192 offset:59392
	v_exp_f32_e32 v210, v26
	v_add_f32_e32 v203, 1.0, v203
	v_add_f32_e32 v204, 1.0, v204
	v_mfma_f32_32x32x16_f16 v[48:63], a[100:103], v[172:175], v[48:63]
	ds_read_b128 v[172:175], v192 offset:60416
	global_load_lds_dwordx4 v192, s[44:45] offset:1024 sc1
	v_exp_f32_e32 v211, v27
	v_add_f32_e32 v205, 1.0, v205
	v_add_f32_e32 v206, 1.0, v206
	v_mfma_f32_32x32x16_f16 v[32:47], a[104:107], v[176:179], v[32:47]
	ds_read_b128 v[176:179], v192 offset:61440
	v_exp_f32_e32 v212, v28
	v_add_f32_e32 v207, 1.0, v207
	v_add_f32_e32 v208, 1.0, v208
	v_mfma_f32_32x32x16_f16 v[48:63], a[104:107], v[180:183], v[48:63]
	ds_read_b128 v[180:183], v192 offset:62464
	v_exp_f32_e32 v213, v29
	v_add_f32_e32 v209, 1.0, v209
	v_add_f32_e32 v210, 1.0, v210
	s_waitcnt lgkmcnt(2)
	v_mfma_f32_32x32x16_f16 v[32:47], a[108:111], v[184:187], v[32:47]
	ds_read_b128 v[184:187], v192 offset:63488
	v_exp_f32_e32 v214, v30
	v_add_f32_e32 v211, 1.0, v211
	v_add_f32_e32 v212, 1.0, v212
	v_mfma_f32_32x32x16_f16 v[48:63], a[108:111], v[188:191], v[48:63]
	ds_read_b128 v[188:191], v192 offset:64512
	global_load_lds_dwordx4 v192, s[44:45] offset:2048 sc1
	v_exp_f32_e32 v215, v31
	v_add_f32_e32 v213, 1.0, v213
	v_add_f32_e32 v214, 1.0, v214
	s_waitcnt vmcnt(7)
	s_barrier
	v_mfma_f32_32x32x16_f16 v[32:47], a[112:115], v[160:163], v[32:47]
	ds_read_b128 v[160:163], v193 offset:0
	v_add_f32_e32 v215, 1.0, v215
	v_rcp_f32_e32 v200, v200
	v_mfma_f32_32x32x16_f16 v[48:63], a[112:115], v[164:167], v[48:63]
	ds_read_b128 v[164:167], v193 offset:1024
	v_rcp_f32_e32 v201, v201
	v_mfma_f32_32x32x16_f16 v[32:47], a[116:119], v[168:171], v[32:47]
	ds_read_b128 v[168:171], v193 offset:2048
	v_rcp_f32_e32 v202, v202
	v_mfma_f32_32x32x16_f16 v[48:63], a[116:119], v[172:175], v[48:63]
	ds_read_b128 v[172:175], v193 offset:3072
	global_load_lds_dwordx4 v192, s[44:45] offset:3072 sc1
	v_rcp_f32_e32 v203, v203
	s_waitcnt lgkmcnt(2)
	v_mfma_f32_32x32x16_f16 v[32:47], a[120:123], v[176:179], v[32:47]
	ds_read_b128 v[176:179], v193 offset:4096
	v_rcp_f32_e32 v204, v204
	s_add_u32 s46, s42, 0x6000
	s_addc_u32 s47, s43, 0
	global_load_dwordx4 v[96:99], v192, s[46:47] offset:0
	v_mfma_f32_32x32x16_f16 v[48:63], a[120:123], v[180:183], v[48:63]
	ds_read_b128 v[180:183], v193 offset:5120
	v_rcp_f32_e32 v205, v205
	v_mul_f32_e32 v204, v204, v132
	global_load_dwordx4 v[100:103], v192, s[46:47] offset:1024
	global_load_dwordx4 v[104:107], v192, s[46:47] offset:2048
	v_mfma_f32_32x32x16_f16 v[32:47], a[124:127], v[184:187], v[32:47]
	ds_read_b128 v[184:187], v193 offset:6144
	v_rcp_f32_e32 v206, v206
	v_mul_f32_e32 v205, v205, v133
	global_load_dwordx4 v[108:111], v192, s[46:47] offset:3072
	s_add_u32 s46, s42, 0x7000
	s_addc_u32 s47, s43, 0
	v_mfma_f32_32x32x16_f16 v[48:63], a[124:127], v[188:191], v[48:63]
	ds_read_b128 v[188:191], v193 offset:7168
	v_cmp_gt_u32_e32 vcc, 3, v251
	s_cbranch_vccnz .LD_tpoll23

.LD_join25:
	s_waitcnt lgkmcnt(3)
	v_mfma_f32_32x32x16_f16 v[32:47], a[180:183], v[168:171], v[32:47]
	ds_read_b128 v[168:171], v193 offset:34816
	v_mfma_f32_32x32x16_f16 v[48:63], a[180:183], v[172:175], v[48:63]
	ds_read_b128 v[172:175], v193 offset:35840
	global_load_lds_dwordx4 v192, s[44:45] offset:3072 sc1
	v_mfma_f32_32x32x16_f16 v[32:47], a[184:187], v[176:179], v[32:47]
	ds_read_b128 v[176:179], v193 offset:36864
	v_mfma_f32_32x32x16_f16 v[48:63], a[184:187], v[180:183], v[48:63]
	ds_read_b128 v[180:183], v193 offset:37888
	v_mfma_f32_32x32x16_f16 v[32:47], a[188:191], v[184:187], v[32:47]
	ds_read_b128 v[184:187], v193 offset:38912
	v_mfma_f32_32x32x16_f16 v[48:63], a[188:191], v[188:191], v[48:63]
	ds_read_b128 v[188:191], v193 offset:39936
	s_mov_b32 m0, s54
	s_add_u32 s44, s34, 0x8000
	s_addc_u32 s45, s35, 0
	global_load_lds_dwordx4 v192, s[44:45] sc1
	s_waitcnt lgkmcnt(2)
	v_mfma_f32_32x32x16_f16 v[32:47], a[192:195], v[160:163], v[32:47]
	ds_read_b128 v[160:163], v193 offset:40960
	v_mfma_f32_32x32x16_f16 v[48:63], a[192:195], v[164:167], v[48:63]
	ds_read_b128 v[164:167], v193 offset:41984
	v_mfma_f32_32x32x16_f16 v[32:47], a[196:199], v[168:171], v[32:47]
	ds_read_b128 v[168:171], v193 offset:43008
	v_mfma_f32_32x32x16_f16 v[48:63], a[196:199], v[172:175], v[48:63]
	ds_read_b128 v[172:175], v193 offset:44032
	global_load_lds_dwordx4 v192, s[44:45] offset:1024 sc1
	v_mfma_f32_32x32x16_f16 v[32:47], a[200:203], v[176:179], v[32:47]
	ds_read_b128 v[176:179], v193 offset:45056
	v_mfma_f32_32x32x16_f16 v[48:63], a[200:203], v[180:183], v[48:63]
	ds_read_b128 v[180:183], v193 offset:46080
	s_waitcnt lgkmcnt(2)
	v_mfma_f32_32x32x16_f16 v[32:47], a[204:207], v[184:187], v[32:47]
	ds_read_b128 v[184:187], v193 offset:47104
	v_mfma_f32_32x32x16_f16 v[48:63], a[204:207], v[188:191], v[48:63]
	ds_read_b128 v[188:191], v193 offset:48128
	global_load_lds_dwordx4 v192, s[44:45] offset:2048 sc1
	v_mfma_f32_32x32x16_f16 v[32:47], a[208:211], v[160:163], v[32:47]
	ds_read_b128 v[160:163], v193 offset:49152
	v_mfma_f32_32x32x16_f16 v[48:63], a[208:211], v[164:167], v[48:63]
	ds_read_b128 v[164:167], v193 offset:50176
	v_mfma_f32_32x32x16_f16 v[32:47], a[212:215], v[168:171], v[32:47]
	ds_read_b128 v[168:171], v193 offset:51200
	v_mfma_f32_32x32x16_f16 v[48:63], a[212:215], v[172:175], v[48:63]
	ds_read_b128 v[172:175], v193 offset:52224
	global_load_lds_dwordx4 v192, s[44:45] offset:3072 sc1
	s_waitcnt lgkmcnt(2)
	v_mfma_f32_32x32x16_f16 v[32:47], a[216:219], v[176:179], v[32:47]
	ds_read_b128 v[176:179], v193 offset:53248
	v_mfma_f32_32x32x16_f16 v[48:63], a[216:219], v[180:183], v[48:63]
	ds_read_b128 v[180:183], v193 offset:54272
	v_mfma_f32_32x32x16_f16 v[32:47], a[220:223], v[184:187], v[32:47]
	ds_read_b128 v[184:187], v193 offset:55296
	s_waitcnt vmcnt(5)
	s_barrier
	v_mov_b32_e32 v199, 1
	s_cmp_eq_u32 s31, 0
	s_cbranch_scc1 .LD_slow26
	global_store_dword v197, v199, s[40:41]
.LD_join27:
	ds_read_b64 v[200:201], v249 offset:0
	ds_read_b64 v[202:203], v249 offset:2048
	ds_read_b64 v[204:205], v249 offset:4096
	ds_read_b64 v[206:207], v249 offset:6144
	v_mfma_f32_32x32x16_f16 v[48:63], a[220:223], v[188:191], v[48:63]
	ds_read_b128 v[188:191], v193 offset:56320
	s_mov_b32 m0, s55
	s_add_u32 s44, s34, 0x9000
	s_addc_u32 s45, s35, 0
	global_load_lds_dwordx4 v192, s[44:45] sc1
	v_mfma_f32_32x32x16_f16 v[32:47], a[224:227], v[160:163], v[32:47]
	ds_read_b128 v[160:163], v193 offset:57344
	v_mfma_f32_32x32x16_f16 v[48:63], a[224:227], v[164:167], v[48:63]
	ds_read_b128 v[164:167], v193 offset:58368
	s_waitcnt lgkmcnt(2)
	v_mfma_f32_32x32x16_f16 v[32:47], a[228:231], v[168:171], v[32:47]
	ds_read_b128 v[168:171], v193 offset:59392
	v_mfma_f32_32x32x16_f16 v[48:63], a[228:231], v[172:175], v[48:63]
	ds_read_b128 v[172:175], v193 offset:60416
	global_load_lds_dwordx4 v192, s[44:45] offset:1024 sc1
	v_mfma_f32_32x32x16_f16 v[32:47], a[232:235], v[176:179], v[32:47]
	ds_read_b128 v[176:179], v193 offset:61440
	v_mfma_f32_32x32x16_f16 v[48:63], a[232:235], v[180:183], v[48:63]
	ds_read_b128 v[180:183], v193 offset:62464
	v_mfma_f32_32x32x16_f16 v[32:47], a[236:239], v[184:187], v[32:47]
	ds_read_b128 v[184:187], v193 offset:63488
	v_mfma_f32_32x32x16_f16 v[48:63], a[236:239], v[188:191], v[48:63]
	ds_read_b128 v[188:191], v193 offset:64512
	global_load_lds_dwordx4 v192, s[44:45] offset:2048 sc1
	s_waitcnt vmcnt(8)
	s_barrier
	s_waitcnt lgkmcnt(2)
	v_mfma_f32_32x32x16_f16 v[32:47], a[240:243], v[160:163], v[32:47]
	ds_read_b128 v[160:163], v192 offset:0
	v_mfma_f32_32x32x16_f16 v[48:63], a[240:243], v[164:167], v[48:63]
	ds_read_b128 v[164:167], v192 offset:1024
	v_mfma_f32_32x32x16_f16 v[32:47], a[244:247], v[168:171], v[32:47]
	ds_read_b128 v[168:171], v192 offset:2048
	v_add_f32_e32 v200, v200, v202
	v_add_f32_e32 v201, v201, v203
	v_add_f32_e32 v200, v200, v204
	v_add_f32_e32 v201, v201, v205
	v_add_f32_e32 v200, v200, v206
	v_add_f32_e32 v201, v201, v207
	global_store_dwordx2 v250, v[200:201], s[72:73]
	v_mfma_f32_32x32x16_f16 v[48:63], a[244:247], v[172:175], v[48:63]
	ds_read_b128 v[172:175], v192 offset:3072
	global_load_lds_dwordx4 v192, s[44:45] offset:3072 sc1
	v_mfma_f32_32x32x16_f16 v[32:47], a[248:251], v[176:179], v[32:47]
	ds_read_b128 v[176:179], v192 offset:4096
	v_mfma_f32_32x32x16_f16 v[48:63], a[248:251], v[180:183], v[48:63]
	ds_read_b128 v[180:183], v192 offset:5120
	s_waitcnt lgkmcnt(2)
	v_mfma_f32_32x32x16_f16 v[32:47], a[252:255], v[184:187], v[32:47]
	ds_read_b128 v[184:187], v192 offset:6144
	s_and_b32 s64, s33, 1
	s_lshl_b32 s64, s64, 22
	s_add_u32 s64, s64, s50
	s_add_u32 s64, s64, 0x20000
	s_add_u32 s36, s6, s64
	s_addc_u32 s37, s7, 0
	s_lshl_b32 s64, s33, 3
	s_add_u32 s64, s64, s29
	s_lshl_b32 s64, s64, 5
	s_add_u32 s64, s64, s30
	s_lshl_b32 s64, s64, 2
	s_add_u32 s40, s8, s64
	s_addc_u32 s41, s9, 0
	s_lshl_b32 s64, s33, 19
	s_add_u32 s64, s64, 0x200
	s_add_u32 s72, s62, s64
	s_addc_u32 s73, s63, 0
	v_mfma_f32_32x32x16_f16 v[48:63], a[252:255], v[188:191], v[48:63]
	ds_read_b128 v[188:191], v192 offset:7168
	s_mov_b32 m0, s56
	s_add_u32 s44, s34, 0x10000
	s_addc_u32 s45, s35, 0
	global_load_lds_dwordx4 v192, s[44:45] sc1
	s_nop 3
	s_waitcnt lgkmcnt(2)
	v_mfma_f32_32x32x16_f16 v[64:79], a[0:3], v[160:163], v[64:79]
	ds_read_b128 v[160:163], v192 offset:8192
	v_exp_f32_e32 v200, v32
	v_mfma_f32_32x32x16_f16 v[80:95], a[0:3], v[164:167], v[80:95]
	ds_read_b128 v[164:167], v192 offset:9216
	s_lshl_b32 s64, s71, 3
	s_add_u32 s64, s64, s29
	s_lshl_b32 s64, s64, 7
	s_add_u32 s38, s8, s64
	s_addc_u32 s39, s9, 0
	global_load_dword v251, v196, s[38:39] sc1
	v_exp_f32_e32 v201, v33
	v_add_f32_e32 v200, 1.0, v200
	v_mfma_f32_32x32x16_f16 v[64:79], a[4:7], v[168:171], v[64:79]
	ds_read_b128 v[168:171], v192 offset:10240
	v_exp_f32_e32 v202, v34
	v_add_f32_e32 v201, 1.0, v201
	v_mfma_f32_32x32x16_f16 v[80:95], a[4:7], v[172:175], v[80:95]
	ds_read_b128 v[172:175], v192 offset:11264
	global_load_lds_dwordx4 v192, s[44:45] offset:1024 sc1
	v_exp_f32_e32 v203, v35
	v_add_f32_e32 v202, 1.0, v202
	v_mfma_f32_32x32x16_f16 v[64:79], a[8:11], v[176:179], v[64:79]
	ds_read_b128 v[176:179], v192 offset:12288
	v_exp_f32_e32 v204, v36
	v_add_f32_e32 v203, 1.0, v203
	v_mfma_f32_32x32x16_f16 v[80:95], a[8:11], v[180:183], v[80:95]
	ds_read_b128 v[180:183], v192 offset:13312
	v_exp_f32_e32 v205, v37
	v_add_f32_e32 v204, 1.0, v204
	s_waitcnt lgkmcnt(2)
	v_mfma_f32_32x32x16_f16 v[64:79], a[12:15], v[184:187], v[64:79]
	ds_read_b128 v[184:187], v192 offset:14336
	v_exp_f32_e32 v206, v38
	v_add_f32_e32 v205, 1.0, v205
	v_mfma_f32_32x32x16_f16 v[80:95], a[12:15], v[188:191], v[80:95]
	ds_read_b128 v[188:191], v192 offset:15360
	global_load_lds_dwordx4 v192, s[44:45] offset:2048 sc1
	v_exp_f32_e32 v207, v39
	v_add_f32_e32 v206, 1.0, v206
	v_mfma_f32_32x32x16_f16 v[64:79], a[16:19], v[160:163], v[64:79]
	ds_read_b128 v[160:163], v192 offset:16384
	v_exp_f32_e32 v208, v40
	v_add_f32_e32 v207, 1.0, v207
	v_mfma_f32_32x32x16_f16 v[80:95], a[16:19], v[164:167], v[80:95]
	ds_read_b128 v[164:167], v192 offset:17408
	v_exp_f32_e32 v209, v41
	v_add_f32_e32 v208, 1.0, v208
	v_mfma_f32_32x32x16_f16 v[64:79], a[20:23], v[168:171], v[64:79]
	ds_read_b128 v[168:171], v192 offset:18432
	v_exp_f32_e32 v210, v42
	v_add_f32_e32 v209, 1.0, v209
	v_mfma_f32_32x32x16_f16 v[80:95], a[20:23], v[172:175], v[80:95]
	ds_read_b128 v[172:175], v192 offset:19456
	global_load_lds_dwordx4 v192, s[44:45] offset:3072 sc1
	v_exp_f32_e32 v211, v43
	v_add_f32_e32 v210, 1.0, v210
	s_waitcnt lgkmcnt(2)
	v_mfma_f32_32x32x16_f16 v[64:79], a[24:27], v[176:179], v[64:79]
	ds_read_b128 v[176:179], v192 offset:20480
	v_exp_f32_e32 v212, v44
	v_add_f32_e32 v211, 1.0, v211
	v_mfma_f32_32x32x16_f16 v[80:95], a[24:27], v[180:183], v[80:95]
	ds_read_b128 v[180:183], v192 offset:21504
	v_exp_f32_e32 v213, v45
	v_add_f32_e32 v212, 1.0, v212
	v_mfma_f32_32x32x16_f16 v[64:79], a[28:31], v[184:187], v[64:79]
	ds_read_b128 v[184:187], v192 offset:22528
	v_exp_f32_e32 v214, v46
	v_add_f32_e32 v213, 1.0, v213
	v_mfma_f32_32x32x16_f16 v[80:95], a[28:31], v[188:191], v[80:95]
	ds_read_b128 v[188:191], v192 offset:23552
	s_mov_b32 m0, s57
	s_add_u32 s44, s34, 0x11000
	s_addc_u32 s45, s35, 0
	global_load_lds_dwordx4 v192, s[44:45] sc1
	v_exp_f32_e32 v215, v47
	v_add_f32_e32 v214, 1.0, v214
	v_mfma_f32_32x32x16_f16 v[64:79], a[32:35], v[160:163], v[64:79]
	ds_read_b128 v[160:163], v192 offset:24576
	v_add_f32_e32 v215, 1.0, v215
	v_rcp_f32_e32 v200, v200
	v_mfma_f32_32x32x16_f16 v[80:95], a[32:35], v[164:167], v[80:95]
	ds_read_b128 v[164:167], v192 offset:25600
	v_rcp_f32_e32 v201, v201
	s_waitcnt lgkmcnt(2)
	v_mfma_f32_32x32x16_f16 v[64:79], a[36:39], v[168:171], v[64:79]
	ds_read_b128 v[168:171], v192 offset:26624
	v_rcp_f32_e32 v202, v202
	v_mfma_f32_32x32x16_f16 v[80:95], a[36:39], v[172:175], v[80:95]
	ds_read_b128 v[172:175], v192 offset:27648
	global_load_lds_dwordx4 v192, s[44:45] offset:1024 sc1
	v_rcp_f32_e32 v203, v203
	v_mfma_f32_32x32x16_f16 v[64:79], a[40:43], v[176:179], v[64:79]
	ds_read_b128 v[176:179], v192 offset:28672
	v_rcp_f32_e32 v204, v204
	v_mfma_f32_32x32x16_f16 v[80:95], a[40:43], v[180:183], v[80:95]
	ds_read_b128 v[180:183], v192 offset:29696
	v_rcp_f32_e32 v205, v205
	v_mul_f32_e32 v204, v204, v136
	v_mfma_f32_32x32x16_f16 v[64:79], a[44:47], v[184:187], v[64:79]
	ds_read_b128 v[184:187], v192 offset:30720
	v_rcp_f32_e32 v206, v206
	v_mul_f32_e32 v205, v205, v137
	v_mfma_f32_32x32x16_f16 v[80:95], a[44:47], v[188:191], v[80:95]
	ds_read_b128 v[188:191], v192 offset:31744
	global_load_lds_dwordx4 v192, s[44:45] offset:2048 sc1
	v_rcp_f32_e32 v207, v207
	v_mul_f32_e32 v206, v206, v138
	s_waitcnt vmcnt(8)
	s_barrier
	s_waitcnt lgkmcnt(2)
	v_mfma_f32_32x32x16_f16 v[64:79], a[48:51], v[160:163], v[64:79]
	ds_read_b128 v[160:163], v192 offset:32768
	v_rcp_f32_e32 v208, v208
	v_mul_f32_e32 v207, v207, v139
	v_mfma_f32_32x32x16_f16 v[80:95], a[48:51], v[164:167], v[80:95]
	ds_read_b128 v[164:167], v192 offset:33792
	v_rcp_f32_e32 v209, v209
	v_fmamk_f32 v208, v208, 0xc0b8aa3b, v198
	v_mfma_f32_32x32x16_f16 v[64:79], a[52:55], v[168:171], v[64:79]
	ds_read_b128 v[168:171], v192 offset:34816
	v_rcp_f32_e32 v210, v210
	v_fmamk_f32 v209, v209, 0xc0b8aa3b, v198
	v_fma_f32 v136, v200, v208, v204
	v_mfma_f32_32x32x16_f16 v[80:95], a[52:55], v[172:175], v[80:95]
	ds_read_b128 v[172:175], v192 offset:35840
	global_load_lds_dwordx4 v192, s[44:45] offset:3072 sc1
	v_rcp_f32_e32 v211, v211
	v_fmamk_f32 v210, v210, 0xc0b8aa3b, v198
	v_fma_f32 v137, v201, v209, v205
	v_mfma_f32_32x32x16_f16 v[64:79], a[56:59], v[176:179], v[64:79]
	ds_read_b128 v[176:179], v192 offset:36864
	v_rcp_f32_e32 v212, v212
	v_fmamk_f32 v211, v211, 0xc0b8aa3b, v198
	v_fma_f32 v138, v202, v210, v206
	v_mfma_f32_32x32x16_f16 v[80:95], a[56:59], v[180:183], v[80:95]
	ds_read_b128 v[180:183], v192 offset:37888
	v_rcp_f32_e32 v213, v213
	v_fma_f32 v139, v203, v211, v207
	s_waitcnt lgkmcnt(2)
	v_mfma_f32_32x32x16_f16 v[64:79], a[60:63], v[184:187], v[64:79]
	ds_read_b128 v[184:187], v192 offset:38912
	v_rcp_f32_e32 v214, v214
	v_mfma_f32_32x32x16_f16 v[80:95], a[60:63], v[188:191], v[80:95]
	ds_read_b128 v[188:191], v192 offset:39936
	s_mov_b32 m0, s58
	s_add_u32 s44, s34, 0x18000
	s_addc_u32 s45, s35, 0
	global_load_lds_dwordx4 v192, s[44:45] sc1
	v_rcp_f32_e32 v215, v215
	v_mfma_f32_32x32x16_f16 v[64:79], a[64:67], v[160:163], v[64:79]
	ds_read_b128 v[160:163], v192 offset:40960
	v_exp_f32_e32 v200, v136
	v_mfma_f32_32x32x16_f16 v[80:95], a[64:67], v[164:167], v[80:95]
	ds_read_b128 v[164:167], v192 offset:41984
	v_exp_f32_e32 v201, v137
	v_add_f32_e32 v200, 1.0, v200
	v_mfma_f32_32x32x16_f16 v[64:79], a[68:71], v[168:171], v[64:79]
	ds_read_b128 v[168:171], v192 offset:43008
	v_exp_f32_e32 v202, v138
	v_add_f32_e32 v201, 1.0, v201
	v_mfma_f32_32x32x16_f16 v[80:95], a[68:71], v[172:175], v[80:95]
	ds_read_b128 v[172:175], v192 offset:44032
	global_load_lds_dwordx4 v192, s[44:45] offset:1024 sc1
	v_exp_f32_e32 v203, v139
	v_add_f32_e32 v202, 1.0, v202
	s_waitcnt lgkmcnt(2)
	v_mfma_f32_32x32x16_f16 v[64:79], a[72:75], v[176:179], v[64:79]
	ds_read_b128 v[176:179], v192 offset:45056
	v_add_f32_e32 v203, 1.0, v203
	v_rcp_f32_e32 v200, v200
	v_mfma_f32_32x32x16_f16 v[80:95], a[72:75], v[180:183], v[80:95]
	ds_read_b128 v[180:183], v192 offset:46080
	v_rcp_f32_e32 v201, v201
	v_fma_f32 v200, v200, 2.0, -1.0
	v_mfma_f32_32x32x16_f16 v[64:79], a[76:79], v[184:187], v[64:79]
	ds_read_b128 v[184:187], v192 offset:47104
	v_rcp_f32_e32 v202, v202
	v_fma_f32 v201, v201, 2.0, -1.0
	v_mul_f32_e32 v216, v212, v200
	v_mfma_f32_32x32x16_f16 v[80:95], a[76:79], v[188:191], v[80:95]
	ds_read_b128 v[188:191], v192 offset:48128
	global_load_lds_dwordx4 v192, s[44:45] offset:2048 sc1
	v_rcp_f32_e32 v203, v203
	v_fma_f32 v202, v202, 2.0, -1.0
	v_mul_f32_e32 v217, v213, v201
	v_mfma_f32_32x32x16_f16 v[64:79], a[80:83], v[160:163], v[64:79]
	ds_read_b128 v[160:163], v192 offset:49152
	v_fma_f32 v203, v203, 2.0, -1.0
	v_mul_f32_e32 v218, v214, v202
	v_exp_f32_e32 v200, v48
	v_mfma_f32_32x32x16_f16 v[80:95], a[80:83], v[164:167], v[80:95]
	ds_read_b128 v[164:167], v192 offset:50176
	v_mul_f32_e32 v219, v215, v203
	v_mul_f32_e32 v236, v216, v228
	v_exp_f32_e32 v201, v49
	s_waitcnt lgkmcnt(2)
	v_mfma_f32_32x32x16_f16 v[64:79], a[84:87], v[168:171], v[64:79]
	ds_read_b128 v[168:171], v192 offset:51200
	v_mul_f32_e32 v237, v216, v232
	v_fmac_f32_e32 v236, v217, v229
	v_exp_f32_e32 v202, v50
	v_mfma_f32_32x32x16_f16 v[80:95], a[84:87], v[172:175], v[80:95]
	ds_read_b128 v[172:175], v192 offset:52224
	global_load_lds_dwordx4 v192, s[44:45] offset:3072 sc1
	v_fmac_f32_e32 v237, v217, v233
	v_fmac_f32_e32 v236, v218, v230
	v_exp_f32_e32 v203, v51
	v_mfma_f32_32x32x16_f16 v[64:79], a[88:91], v[176:179], v[64:79]
	ds_read_b128 v[176:179], v192 offset:53248
	v_fmac_f32_e32 v237, v218, v234
	v_fmac_f32_e32 v236, v219, v231
	v_exp_f32_e32 v204, v52
	v_mfma_f32_32x32x16_f16 v[80:95], a[88:91], v[180:183], v[80:95]
	ds_read_b128 v[180:183], v192 offset:54272
	v_fmac_f32_e32 v237, v219, v235
	v_mov_b32_e32 v238, v236
	v_exp_f32_e32 v205, v53
	v_mfma_f32_32x32x16_f16 v[64:79], a[92:95], v[184:187], v[64:79]
	ds_read_b128 v[184:187], v192 offset:55296
	v_mov_b32_e32 v240, v237
	v_cvt_pk_f16_f32 v220, v216, v217
	v_exp_f32_e32 v206, v54
	v_mfma_f32_32x32x16_f16 v[80:95], a[92:95], v[188:191], v[80:95]
	ds_read_b128 v[188:191], v192 offset:56320
	s_mov_b32 m0, s59
	s_add_u32 s44, s34, 0x19000
	s_addc_u32 s45, s35, 0
	global_load_lds_dwordx4 v192, s[44:45] sc1
	v_permlane32_swap_b32_e32 v236, v238
	v_permlane32_swap_b32_e32 v237, v240
	v_add_f32_e32 v238, v236, v238
	v_add_f32_e32 v239, v237, v240
	ds_write_b64 v248, v[238:239] offset:512
	v_exp_f32_e32 v207, v55
	s_waitcnt lgkmcnt(3)
	v_mfma_f32_32x32x16_f16 v[64:79], a[96:99], v[160:163], v[64:79]
	ds_read_b128 v[160:163], v192 offset:57344
	v_cvt_pk_f16_f32 v221, v218, v219
	v_exp_f32_e32 v208, v56
	v_add_f32_e32 v200, 1.0, v200
	v_mfma_f32_32x32x16_f16 v[80:95], a[96:99], v[164:167], v[80:95]
	ds_read_b128 v[164:167], v192 offset:58368
	v_exp_f32_e32 v209, v57
	v_add_f32_e32 v201, 1.0, v201
	v_add_f32_e32 v202, 1.0, v202
	v_mfma_f32_32x32x16_f16 v[64:79], a[100:103], v[168:171], v[64:79]
	ds_read_b128 v[168:171], v192 offset:59392
	v_exp_f32_e32 v210, v58
	v_add_f32_e32 v203, 1.0, v203
	v_add_f32_e32 v204, 1.0, v204
	v_mfma_f32_32x32x16_f16 v[80:95], a[100:103], v[172:175], v[80:95]
	ds_read_b128 v[172:175], v192 offset:60416
	global_load_lds_dwordx4 v192, s[44:45] offset:1024 sc1
	v_exp_f32_e32 v211, v59
	v_add_f32_e32 v205, 1.0, v205
	v_add_f32_e32 v206, 1.0, v206
	v_mfma_f32_32x32x16_f16 v[64:79], a[104:107], v[176:179], v[64:79]
	ds_read_b128 v[176:179], v192 offset:61440
	v_exp_f32_e32 v212, v60
	v_add_f32_e32 v207, 1.0, v207
	v_add_f32_e32 v208, 1.0, v208
	v_mfma_f32_32x32x16_f16 v[80:95], a[104:107], v[180:183], v[80:95]
	ds_read_b128 v[180:183], v192 offset:62464
	v_exp_f32_e32 v213, v61
	v_add_f32_e32 v209, 1.0, v209
	v_add_f32_e32 v210, 1.0, v210
	s_waitcnt lgkmcnt(2)
	v_mfma_f32_32x32x16_f16 v[64:79], a[108:111], v[184:187], v[64:79]
	ds_read_b128 v[184:187], v192 offset:63488
	v_exp_f32_e32 v214, v62
	v_add_f32_e32 v211, 1.0, v211
	v_add_f32_e32 v212, 1.0, v212
	v_mfma_f32_32x32x16_f16 v[80:95], a[108:111], v[188:191], v[80:95]
	ds_read_b128 v[188:191], v192 offset:64512
	global_load_lds_dwordx4 v192, s[44:45] offset:2048 sc1
	v_exp_f32_e32 v215, v63
	v_add_f32_e32 v213, 1.0, v213
	v_add_f32_e32 v214, 1.0, v214
	s_waitcnt vmcnt(7)
	s_barrier
	v_mfma_f32_32x32x16_f16 v[64:79], a[112:115], v[160:163], v[64:79]
	ds_read_b128 v[160:163], v193 offset:0
	v_add_f32_e32 v215, 1.0, v215
	v_rcp_f32_e32 v200, v200
	v_mfma_f32_32x32x16_f16 v[80:95], a[112:115], v[164:167], v[80:95]
	ds_read_b128 v[164:167], v193 offset:1024
	v_rcp_f32_e32 v201, v201
	v_mfma_f32_32x32x16_f16 v[64:79], a[116:119], v[168:171], v[64:79]
	ds_read_b128 v[168:171], v193 offset:2048
	v_rcp_f32_e32 v202, v202
	v_mfma_f32_32x32x16_f16 v[80:95], a[116:119], v[172:175], v[80:95]
	ds_read_b128 v[172:175], v193 offset:3072
	global_load_lds_dwordx4 v192, s[44:45] offset:3072 sc1
	v_rcp_f32_e32 v203, v203
	s_waitcnt lgkmcnt(2)
	v_mfma_f32_32x32x16_f16 v[64:79], a[120:123], v[176:179], v[64:79]
	ds_read_b128 v[176:179], v193 offset:4096
	v_rcp_f32_e32 v204, v204
	s_add_u32 s46, s42, 0x0
	s_addc_u32 s47, s43, 0
	global_load_dwordx4 v[0:3], v192, s[46:47] offset:0
	v_mfma_f32_32x32x16_f16 v[80:95], a[120:123], v[180:183], v[80:95]
	ds_read_b128 v[180:183], v193 offset:5120
	v_rcp_f32_e32 v205, v205
	v_mul_f32_e32 v204, v204, v140
	global_load_dwordx4 v[4:7], v192, s[46:47] offset:1024
	global_load_dwordx4 v[8:11], v192, s[46:47] offset:2048
	v_mfma_f32_32x32x16_f16 v[64:79], a[124:127], v[184:187], v[64:79]
	ds_read_b128 v[184:187], v193 offset:6144
	v_rcp_f32_e32 v206, v206
	v_mul_f32_e32 v205, v205, v141
	global_load_dwordx4 v[12:15], v192, s[46:47] offset:3072
	s_add_u32 s46, s42, 0x1000
	s_addc_u32 s47, s43, 0
	v_mfma_f32_32x32x16_f16 v[80:95], a[124:127], v[188:191], v[80:95]
	ds_read_b128 v[188:191], v193 offset:7168
	v_cmp_gt_u32_e32 vcc, 4, v251
	s_cbranch_vccnz .LD_tpoll29

.LD_join31:
	s_waitcnt lgkmcnt(3)
	v_mfma_f32_32x32x16_f16 v[64:79], a[180:183], v[168:171], v[64:79]
	ds_read_b128 v[168:171], v193 offset:34816
	v_mfma_f32_32x32x16_f16 v[80:95], a[180:183], v[172:175], v[80:95]
	ds_read_b128 v[172:175], v193 offset:35840
	global_load_lds_dwordx4 v192, s[44:45] offset:3072 sc1
	v_mfma_f32_32x32x16_f16 v[64:79], a[184:187], v[176:179], v[64:79]
	ds_read_b128 v[176:179], v193 offset:36864
	v_mfma_f32_32x32x16_f16 v[80:95], a[184:187], v[180:183], v[80:95]
	ds_read_b128 v[180:183], v193 offset:37888
	v_mfma_f32_32x32x16_f16 v[64:79], a[188:191], v[184:187], v[64:79]
	ds_read_b128 v[184:187], v193 offset:38912
	v_mfma_f32_32x32x16_f16 v[80:95], a[188:191], v[188:191], v[80:95]
	ds_read_b128 v[188:191], v193 offset:39936
	s_mov_b32 m0, s54
	s_add_u32 s44, s34, 0x8000
	s_addc_u32 s45, s35, 0
	global_load_lds_dwordx4 v192, s[44:45] sc1
	s_waitcnt lgkmcnt(2)
	v_mfma_f32_32x32x16_f16 v[64:79], a[192:195], v[160:163], v[64:79]
	ds_read_b128 v[160:163], v193 offset:40960
	v_mfma_f32_32x32x16_f16 v[80:95], a[192:195], v[164:167], v[80:95]
	ds_read_b128 v[164:167], v193 offset:41984
	v_mfma_f32_32x32x16_f16 v[64:79], a[196:199], v[168:171], v[64:79]
	ds_read_b128 v[168:171], v193 offset:43008
	v_mfma_f32_32x32x16_f16 v[80:95], a[196:199], v[172:175], v[80:95]
	ds_read_b128 v[172:175], v193 offset:44032
	global_load_lds_dwordx4 v192, s[44:45] offset:1024 sc1
	v_mfma_f32_32x32x16_f16 v[64:79], a[200:203], v[176:179], v[64:79]
	ds_read_b128 v[176:179], v193 offset:45056
	v_mfma_f32_32x32x16_f16 v[80:95], a[200:203], v[180:183], v[80:95]
	ds_read_b128 v[180:183], v193 offset:46080
	s_waitcnt lgkmcnt(2)
	v_mfma_f32_32x32x16_f16 v[64:79], a[204:207], v[184:187], v[64:79]
	ds_read_b128 v[184:187], v193 offset:47104
	v_mfma_f32_32x32x16_f16 v[80:95], a[204:207], v[188:191], v[80:95]
	ds_read_b128 v[188:191], v193 offset:48128
	global_load_lds_dwordx4 v192, s[44:45] offset:2048 sc1
	v_mfma_f32_32x32x16_f16 v[64:79], a[208:211], v[160:163], v[64:79]
	ds_read_b128 v[160:163], v193 offset:49152
	v_mfma_f32_32x32x16_f16 v[80:95], a[208:211], v[164:167], v[80:95]
	ds_read_b128 v[164:167], v193 offset:50176
	v_mfma_f32_32x32x16_f16 v[64:79], a[212:215], v[168:171], v[64:79]
	ds_read_b128 v[168:171], v193 offset:51200
	v_mfma_f32_32x32x16_f16 v[80:95], a[212:215], v[172:175], v[80:95]
	ds_read_b128 v[172:175], v193 offset:52224
	global_load_lds_dwordx4 v192, s[44:45] offset:3072 sc1
	s_waitcnt lgkmcnt(2)
	v_mfma_f32_32x32x16_f16 v[64:79], a[216:219], v[176:179], v[64:79]
	ds_read_b128 v[176:179], v193 offset:53248
	v_mfma_f32_32x32x16_f16 v[80:95], a[216:219], v[180:183], v[80:95]
	ds_read_b128 v[180:183], v193 offset:54272
	v_mfma_f32_32x32x16_f16 v[64:79], a[220:223], v[184:187], v[64:79]
	ds_read_b128 v[184:187], v193 offset:55296
	s_waitcnt vmcnt(5)
	s_barrier
	v_mov_b32_e32 v199, 2
	s_cmp_eq_u32 s31, 0
	s_cbranch_scc1 .LD_slow32
	global_store_dword v197, v199, s[40:41]
.LD_join33:
	ds_read_b64 v[200:201], v249 offset:512
	ds_read_b64 v[202:203], v249 offset:2560
	ds_read_b64 v[204:205], v249 offset:4608
	ds_read_b64 v[206:207], v249 offset:6656
	v_mfma_f32_32x32x16_f16 v[80:95], a[220:223], v[188:191], v[80:95]
	ds_read_b128 v[188:191], v193 offset:56320
	s_mov_b32 m0, s55
	s_add_u32 s44, s34, 0x9000
	s_addc_u32 s45, s35, 0
	global_load_lds_dwordx4 v192, s[44:45] sc1
	v_mfma_f32_32x32x16_f16 v[64:79], a[224:227], v[160:163], v[64:79]
	ds_read_b128 v[160:163], v193 offset:57344
	v_mfma_f32_32x32x16_f16 v[80:95], a[224:227], v[164:167], v[80:95]
	ds_read_b128 v[164:167], v193 offset:58368
	s_waitcnt lgkmcnt(2)
	v_mfma_f32_32x32x16_f16 v[64:79], a[228:231], v[168:171], v[64:79]
	ds_read_b128 v[168:171], v193 offset:59392
	v_mfma_f32_32x32x16_f16 v[80:95], a[228:231], v[172:175], v[80:95]
	ds_read_b128 v[172:175], v193 offset:60416
	global_load_lds_dwordx4 v192, s[44:45] offset:1024 sc1
	v_mfma_f32_32x32x16_f16 v[64:79], a[232:235], v[176:179], v[64:79]
	ds_read_b128 v[176:179], v193 offset:61440
	v_mfma_f32_32x32x16_f16 v[80:95], a[232:235], v[180:183], v[80:95]
	ds_read_b128 v[180:183], v193 offset:62464
	v_mfma_f32_32x32x16_f16 v[64:79], a[236:239], v[184:187], v[64:79]
	ds_read_b128 v[184:187], v193 offset:63488
	v_mfma_f32_32x32x16_f16 v[80:95], a[236:239], v[188:191], v[80:95]
	ds_read_b128 v[188:191], v193 offset:64512
	global_load_lds_dwordx4 v192, s[44:45] offset:2048 sc1
	s_waitcnt vmcnt(8)
	s_barrier
	s_waitcnt lgkmcnt(2)
	v_mfma_f32_32x32x16_f16 v[64:79], a[240:243], v[160:163], v[64:79]
	ds_read_b128 v[160:163], v192 offset:0
	v_mfma_f32_32x32x16_f16 v[80:95], a[240:243], v[164:167], v[80:95]
	ds_read_b128 v[164:167], v192 offset:1024
	v_mfma_f32_32x32x16_f16 v[64:79], a[244:247], v[168:171], v[64:79]
	ds_read_b128 v[168:171], v192 offset:2048
	v_add_f32_e32 v200, v200, v202
	v_add_f32_e32 v201, v201, v203
	v_add_f32_e32 v200, v200, v204
	v_add_f32_e32 v201, v201, v205
	v_add_f32_e32 v200, v200, v206
	v_add_f32_e32 v201, v201, v207
	global_store_dwordx2 v250, v[200:201], s[72:73]
	v_mfma_f32_32x32x16_f16 v[80:95], a[244:247], v[172:175], v[80:95]
	ds_read_b128 v[172:175], v192 offset:3072
	global_load_lds_dwordx4 v192, s[44:45] offset:3072 sc1
	v_mfma_f32_32x32x16_f16 v[64:79], a[248:251], v[176:179], v[64:79]
	ds_read_b128 v[176:179], v192 offset:4096
	v_mfma_f32_32x32x16_f16 v[80:95], a[248:251], v[180:183], v[80:95]
	ds_read_b128 v[180:183], v192 offset:5120
	s_waitcnt lgkmcnt(2)
	v_mfma_f32_32x32x16_f16 v[64:79], a[252:255], v[184:187], v[64:79]
	ds_read_b128 v[184:187], v192 offset:6144
	s_and_b32 s64, s33, 1
	s_lshl_b32 s64, s64, 22
	s_add_u32 s64, s64, s50
	s_add_u32 s64, s64, 0x40000
	s_add_u32 s36, s6, s64
	s_addc_u32 s37, s7, 0
	s_lshl_b32 s64, s33, 3
	s_add_u32 s64, s64, s29
	s_lshl_b32 s64, s64, 5
	s_add_u32 s64, s64, s30
	s_lshl_b32 s64, s64, 2
	s_add_u32 s40, s8, s64
	s_addc_u32 s41, s9, 0
	s_lshl_b32 s64, s33, 19
	s_add_u32 s64, s64, 0x400
	s_add_u32 s72, s62, s64
	s_addc_u32 s73, s63, 0
	v_mfma_f32_32x32x16_f16 v[80:95], a[252:255], v[188:191], v[80:95]
	ds_read_b128 v[188:191], v192 offset:7168
	s_mov_b32 m0, s56
	s_add_u32 s44, s34, 0x10000
	s_addc_u32 s45, s35, 0
	global_load_lds_dwordx4 v192, s[44:45] sc1
	s_nop 3
	s_waitcnt lgkmcnt(2)
	v_mfma_f32_32x32x16_f16 v[96:111], a[0:3], v[160:163], v[96:111]
	ds_read_b128 v[160:163], v192 offset:8192
	v_exp_f32_e32 v200, v64
	v_mfma_f32_32x32x16_f16 v[112:127], a[0:3], v[164:167], v[112:127]
	ds_read_b128 v[164:167], v192 offset:9216
	s_lshl_b32 s64, s33, 3
	s_add_u32 s64, s64, s29
	s_lshl_b32 s64, s64, 7
	s_add_u32 s38, s8, s64
	s_addc_u32 s39, s9, 0
	global_load_dword v251, v196, s[38:39] sc1
	v_exp_f32_e32 v201, v65
	v_add_f32_e32 v200, 1.0, v200
	v_mfma_f32_32x32x16_f16 v[96:111], a[4:7], v[168:171], v[96:111]
	ds_read_b128 v[168:171], v192 offset:10240
	v_exp_f32_e32 v202, v66
	v_add_f32_e32 v201, 1.0, v201
	v_mfma_f32_32x32x16_f16 v[112:127], a[4:7], v[172:175], v[112:127]
	ds_read_b128 v[172:175], v192 offset:11264
	global_load_lds_dwordx4 v192, s[44:45] offset:1024 sc1
	v_exp_f32_e32 v203, v67
	v_add_f32_e32 v202, 1.0, v202
	v_mfma_f32_32x32x16_f16 v[96:111], a[8:11], v[176:179], v[96:111]
	ds_read_b128 v[176:179], v192 offset:12288
	v_exp_f32_e32 v204, v68
	v_add_f32_e32 v203, 1.0, v203
	v_mfma_f32_32x32x16_f16 v[112:127], a[8:11], v[180:183], v[112:127]
	ds_read_b128 v[180:183], v192 offset:13312
	v_exp_f32_e32 v205, v69
	v_add_f32_e32 v204, 1.0, v204
	s_waitcnt lgkmcnt(2)
	v_mfma_f32_32x32x16_f16 v[96:111], a[12:15], v[184:187], v[96:111]
	ds_read_b128 v[184:187], v192 offset:14336
	v_exp_f32_e32 v206, v70
	v_add_f32_e32 v205, 1.0, v205
	v_mfma_f32_32x32x16_f16 v[112:127], a[12:15], v[188:191], v[112:127]
	ds_read_b128 v[188:191], v192 offset:15360
	global_load_lds_dwordx4 v192, s[44:45] offset:2048 sc1
	v_exp_f32_e32 v207, v71
	v_add_f32_e32 v206, 1.0, v206
	v_mfma_f32_32x32x16_f16 v[96:111], a[16:19], v[160:163], v[96:111]
	ds_read_b128 v[160:163], v192 offset:16384
	v_exp_f32_e32 v208, v72
	v_add_f32_e32 v207, 1.0, v207
	v_mfma_f32_32x32x16_f16 v[112:127], a[16:19], v[164:167], v[112:127]
	ds_read_b128 v[164:167], v192 offset:17408
	v_exp_f32_e32 v209, v73
	v_add_f32_e32 v208, 1.0, v208
	v_mfma_f32_32x32x16_f16 v[96:111], a[20:23], v[168:171], v[96:111]
	ds_read_b128 v[168:171], v192 offset:18432
	v_exp_f32_e32 v210, v74
	v_add_f32_e32 v209, 1.0, v209
	v_mfma_f32_32x32x16_f16 v[112:127], a[20:23], v[172:175], v[112:127]
	ds_read_b128 v[172:175], v192 offset:19456
	global_load_lds_dwordx4 v192, s[44:45] offset:3072 sc1
	v_exp_f32_e32 v211, v75
	v_add_f32_e32 v210, 1.0, v210
	s_waitcnt lgkmcnt(2)
	v_mfma_f32_32x32x16_f16 v[96:111], a[24:27], v[176:179], v[96:111]
	ds_read_b128 v[176:179], v192 offset:20480
	v_exp_f32_e32 v212, v76
	v_add_f32_e32 v211, 1.0, v211
	v_mfma_f32_32x32x16_f16 v[112:127], a[24:27], v[180:183], v[112:127]
	ds_read_b128 v[180:183], v192 offset:21504
	v_exp_f32_e32 v213, v77
	v_add_f32_e32 v212, 1.0, v212
	v_mfma_f32_32x32x16_f16 v[96:111], a[28:31], v[184:187], v[96:111]
	ds_read_b128 v[184:187], v192 offset:22528
	v_exp_f32_e32 v214, v78
	v_add_f32_e32 v213, 1.0, v213
	v_mfma_f32_32x32x16_f16 v[112:127], a[28:31], v[188:191], v[112:127]
	ds_read_b128 v[188:191], v192 offset:23552
	s_mov_b32 m0, s57
	s_add_u32 s44, s34, 0x11000
	s_addc_u32 s45, s35, 0
	global_load_lds_dwordx4 v192, s[44:45] sc1
	v_exp_f32_e32 v215, v79
	v_add_f32_e32 v214, 1.0, v214
	v_mfma_f32_32x32x16_f16 v[96:111], a[32:35], v[160:163], v[96:111]
	ds_read_b128 v[160:163], v192 offset:24576
	v_add_f32_e32 v215, 1.0, v215
	v_rcp_f32_e32 v200, v200
	v_mfma_f32_32x32x16_f16 v[112:127], a[32:35], v[164:167], v[112:127]
	ds_read_b128 v[164:167], v192 offset:25600
	v_rcp_f32_e32 v201, v201
	s_waitcnt lgkmcnt(2)
	v_mfma_f32_32x32x16_f16 v[96:111], a[36:39], v[168:171], v[96:111]
	ds_read_b128 v[168:171], v192 offset:26624
	v_rcp_f32_e32 v202, v202
	v_mfma_f32_32x32x16_f16 v[112:127], a[36:39], v[172:175], v[112:127]
	ds_read_b128 v[172:175], v192 offset:27648
	global_load_lds_dwordx4 v192, s[44:45] offset:1024 sc1
	v_rcp_f32_e32 v203, v203
	v_mfma_f32_32x32x16_f16 v[96:111], a[40:43], v[176:179], v[96:111]
	ds_read_b128 v[176:179], v192 offset:28672
	v_rcp_f32_e32 v204, v204
	v_mfma_f32_32x32x16_f16 v[112:127], a[40:43], v[180:183], v[112:127]
	ds_read_b128 v[180:183], v192 offset:29696
	v_rcp_f32_e32 v205, v205
	v_mul_f32_e32 v204, v204, v144
	v_mfma_f32_32x32x16_f16 v[96:111], a[44:47], v[184:187], v[96:111]
	ds_read_b128 v[184:187], v192 offset:30720
	v_rcp_f32_e32 v206, v206
	v_mul_f32_e32 v205, v205, v145
	v_mfma_f32_32x32x16_f16 v[112:127], a[44:47], v[188:191], v[112:127]
	ds_read_b128 v[188:191], v192 offset:31744
	global_load_lds_dwordx4 v192, s[44:45] offset:2048 sc1
	v_rcp_f32_e32 v207, v207
	v_mul_f32_e32 v206, v206, v146
	s_waitcnt vmcnt(8)
	s_barrier
	s_waitcnt lgkmcnt(2)
	v_mfma_f32_32x32x16_f16 v[96:111], a[48:51], v[160:163], v[96:111]
	ds_read_b128 v[160:163], v192 offset:32768
	v_rcp_f32_e32 v208, v208
	v_mul_f32_e32 v207, v207, v147
	v_mfma_f32_32x32x16_f16 v[112:127], a[48:51], v[164:167], v[112:127]
	ds_read_b128 v[164:167], v192 offset:33792
	v_rcp_f32_e32 v209, v209
	v_fmamk_f32 v208, v208, 0xc0b8aa3b, v198
	v_mfma_f32_32x32x16_f16 v[96:111], a[52:55], v[168:171], v[96:111]
	ds_read_b128 v[168:171], v192 offset:34816
	v_rcp_f32_e32 v210, v210
	v_fmamk_f32 v209, v209, 0xc0b8aa3b, v198
	v_fma_f32 v144, v200, v208, v204
	v_mfma_f32_32x32x16_f16 v[112:127], a[52:55], v[172:175], v[112:127]
	ds_read_b128 v[172:175], v192 offset:35840
	global_load_lds_dwordx4 v192, s[44:45] offset:3072 sc1
	v_rcp_f32_e32 v211, v211
	v_fmamk_f32 v210, v210, 0xc0b8aa3b, v198
	v_fma_f32 v145, v201, v209, v205
	v_mfma_f32_32x32x16_f16 v[96:111], a[56:59], v[176:179], v[96:111]
	ds_read_b128 v[176:179], v192 offset:36864
	v_rcp_f32_e32 v212, v212
	v_fmamk_f32 v211, v211, 0xc0b8aa3b, v198
	v_fma_f32 v146, v202, v210, v206
	v_mfma_f32_32x32x16_f16 v[112:127], a[56:59], v[180:183], v[112:127]
	ds_read_b128 v[180:183], v192 offset:37888
	v_rcp_f32_e32 v213, v213
	v_fma_f32 v147, v203, v211, v207
	s_waitcnt lgkmcnt(2)
	v_mfma_f32_32x32x16_f16 v[96:111], a[60:63], v[184:187], v[96:111]
	ds_read_b128 v[184:187], v192 offset:38912
	v_rcp_f32_e32 v214, v214
	v_mfma_f32_32x32x16_f16 v[112:127], a[60:63], v[188:191], v[112:127]
	ds_read_b128 v[188:191], v192 offset:39936
	s_mov_b32 m0, s58
	s_add_u32 s44, s34, 0x18000
	s_addc_u32 s45, s35, 0
	global_load_lds_dwordx4 v192, s[44:45] sc1
	v_rcp_f32_e32 v215, v215
	v_mfma_f32_32x32x16_f16 v[96:111], a[64:67], v[160:163], v[96:111]
	ds_read_b128 v[160:163], v192 offset:40960
	v_exp_f32_e32 v200, v144
	v_mfma_f32_32x32x16_f16 v[112:127], a[64:67], v[164:167], v[112:127]
	ds_read_b128 v[164:167], v192 offset:41984
	v_exp_f32_e32 v201, v145
	v_add_f32_e32 v200, 1.0, v200
	v_mfma_f32_32x32x16_f16 v[96:111], a[68:71], v[168:171], v[96:111]
	ds_read_b128 v[168:171], v192 offset:43008
	v_exp_f32_e32 v202, v146
	v_add_f32_e32 v201, 1.0, v201
	v_mfma_f32_32x32x16_f16 v[112:127], a[68:71], v[172:175], v[112:127]
	ds_read_b128 v[172:175], v192 offset:44032
	global_load_lds_dwordx4 v192, s[44:45] offset:1024 sc1
	v_exp_f32_e32 v203, v147
	v_add_f32_e32 v202, 1.0, v202
	s_waitcnt lgkmcnt(2)
	v_mfma_f32_32x32x16_f16 v[96:111], a[72:75], v[176:179], v[96:111]
	ds_read_b128 v[176:179], v192 offset:45056
	v_add_f32_e32 v203, 1.0, v203
	v_rcp_f32_e32 v200, v200
	v_mfma_f32_32x32x16_f16 v[112:127], a[72:75], v[180:183], v[112:127]
	ds_read_b128 v[180:183], v192 offset:46080
	v_rcp_f32_e32 v201, v201
	v_fma_f32 v200, v200, 2.0, -1.0
	v_mfma_f32_32x32x16_f16 v[96:111], a[76:79], v[184:187], v[96:111]
	ds_read_b128 v[184:187], v192 offset:47104
	v_rcp_f32_e32 v202, v202
	v_fma_f32 v201, v201, 2.0, -1.0
	v_mul_f32_e32 v216, v212, v200
	v_mfma_f32_32x32x16_f16 v[112:127], a[76:79], v[188:191], v[112:127]
	ds_read_b128 v[188:191], v192 offset:48128
	global_load_lds_dwordx4 v192, s[44:45] offset:2048 sc1
	v_rcp_f32_e32 v203, v203
	v_fma_f32 v202, v202, 2.0, -1.0
	v_mul_f32_e32 v217, v213, v201
	v_mfma_f32_32x32x16_f16 v[96:111], a[80:83], v[160:163], v[96:111]
	ds_read_b128 v[160:163], v192 offset:49152
	v_fma_f32 v203, v203, 2.0, -1.0
	v_mul_f32_e32 v218, v214, v202
	v_exp_f32_e32 v200, v80
	v_mfma_f32_32x32x16_f16 v[112:127], a[80:83], v[164:167], v[112:127]
	ds_read_b128 v[164:167], v192 offset:50176
	v_mul_f32_e32 v219, v215, v203
	v_mul_f32_e32 v236, v216, v228
	v_exp_f32_e32 v201, v81
	s_waitcnt lgkmcnt(2)
	v_mfma_f32_32x32x16_f16 v[96:111], a[84:87], v[168:171], v[96:111]
	ds_read_b128 v[168:171], v192 offset:51200
	v_mul_f32_e32 v237, v216, v232
	v_fmac_f32_e32 v236, v217, v229
	v_exp_f32_e32 v202, v82
	v_mfma_f32_32x32x16_f16 v[112:127], a[84:87], v[172:175], v[112:127]
	ds_read_b128 v[172:175], v192 offset:52224
	global_load_lds_dwordx4 v192, s[44:45] offset:3072 sc1
	v_fmac_f32_e32 v237, v217, v233
	v_fmac_f32_e32 v236, v218, v230
	v_exp_f32_e32 v203, v83
	v_mfma_f32_32x32x16_f16 v[96:111], a[88:91], v[176:179], v[96:111]
	ds_read_b128 v[176:179], v192 offset:53248
	v_fmac_f32_e32 v237, v218, v234
	v_fmac_f32_e32 v236, v219, v231
	v_exp_f32_e32 v204, v84
	v_mfma_f32_32x32x16_f16 v[112:127], a[88:91], v[180:183], v[112:127]
	ds_read_b128 v[180:183], v192 offset:54272
	v_fmac_f32_e32 v237, v219, v235
	v_mov_b32_e32 v238, v236
	v_exp_f32_e32 v205, v85
	v_mfma_f32_32x32x16_f16 v[96:111], a[92:95], v[184:187], v[96:111]
	ds_read_b128 v[184:187], v192 offset:55296
	v_mov_b32_e32 v240, v237
	v_cvt_pk_f16_f32 v220, v216, v217
	v_exp_f32_e32 v206, v86
	v_mfma_f32_32x32x16_f16 v[112:127], a[92:95], v[188:191], v[112:127]
	ds_read_b128 v[188:191], v192 offset:56320
	s_mov_b32 m0, s59
	s_add_u32 s44, s34, 0x19000
	s_addc_u32 s45, s35, 0
	global_load_lds_dwordx4 v192, s[44:45] sc1
	v_permlane32_swap_b32_e32 v236, v238
	v_permlane32_swap_b32_e32 v237, v240
	v_add_f32_e32 v238, v236, v238
	v_add_f32_e32 v239, v237, v240
	ds_write_b64 v248, v[238:239] offset:1024
	v_exp_f32_e32 v207, v87
	s_waitcnt lgkmcnt(3)
	v_mfma_f32_32x32x16_f16 v[96:111], a[96:99], v[160:163], v[96:111]
	ds_read_b128 v[160:163], v192 offset:57344
	v_cvt_pk_f16_f32 v221, v218, v219
	v_exp_f32_e32 v208, v88
	v_add_f32_e32 v200, 1.0, v200
	v_mfma_f32_32x32x16_f16 v[112:127], a[96:99], v[164:167], v[112:127]
	ds_read_b128 v[164:167], v192 offset:58368
	v_exp_f32_e32 v209, v89
	v_add_f32_e32 v201, 1.0, v201
	v_add_f32_e32 v202, 1.0, v202
	v_mfma_f32_32x32x16_f16 v[96:111], a[100:103], v[168:171], v[96:111]
	ds_read_b128 v[168:171], v192 offset:59392
	v_exp_f32_e32 v210, v90
	v_add_f32_e32 v203, 1.0, v203
	v_add_f32_e32 v204, 1.0, v204
	v_mfma_f32_32x32x16_f16 v[112:127], a[100:103], v[172:175], v[112:127]
	ds_read_b128 v[172:175], v192 offset:60416
	global_load_lds_dwordx4 v192, s[44:45] offset:1024 sc1
	v_exp_f32_e32 v211, v91
	v_add_f32_e32 v205, 1.0, v205
	v_add_f32_e32 v206, 1.0, v206
	v_mfma_f32_32x32x16_f16 v[96:111], a[104:107], v[176:179], v[96:111]
	ds_read_b128 v[176:179], v192 offset:61440
	v_exp_f32_e32 v212, v92
	v_add_f32_e32 v207, 1.0, v207
	v_add_f32_e32 v208, 1.0, v208
	v_mfma_f32_32x32x16_f16 v[112:127], a[104:107], v[180:183], v[112:127]
	ds_read_b128 v[180:183], v192 offset:62464
	v_exp_f32_e32 v213, v93
	v_add_f32_e32 v209, 1.0, v209
	v_add_f32_e32 v210, 1.0, v210
	s_waitcnt lgkmcnt(2)
	v_mfma_f32_32x32x16_f16 v[96:111], a[108:111], v[184:187], v[96:111]
	ds_read_b128 v[184:187], v192 offset:63488
	v_exp_f32_e32 v214, v94
	v_add_f32_e32 v211, 1.0, v211
	v_add_f32_e32 v212, 1.0, v212
	v_mfma_f32_32x32x16_f16 v[112:127], a[108:111], v[188:191], v[112:127]
	ds_read_b128 v[188:191], v192 offset:64512
	global_load_lds_dwordx4 v192, s[44:45] offset:2048 sc1
	v_exp_f32_e32 v215, v95
	v_add_f32_e32 v213, 1.0, v213
	v_add_f32_e32 v214, 1.0, v214
	s_waitcnt vmcnt(7)
	s_barrier
	v_mfma_f32_32x32x16_f16 v[96:111], a[112:115], v[160:163], v[96:111]
	ds_read_b128 v[160:163], v193 offset:0
	v_add_f32_e32 v215, 1.0, v215
	v_rcp_f32_e32 v200, v200
	v_mfma_f32_32x32x16_f16 v[112:127], a[112:115], v[164:167], v[112:127]
	ds_read_b128 v[164:167], v193 offset:1024
	v_rcp_f32_e32 v201, v201
	v_mfma_f32_32x32x16_f16 v[96:111], a[116:119], v[168:171], v[96:111]
	ds_read_b128 v[168:171], v193 offset:2048
	v_rcp_f32_e32 v202, v202
	v_mfma_f32_32x32x16_f16 v[112:127], a[116:119], v[172:175], v[112:127]
	ds_read_b128 v[172:175], v193 offset:3072
	global_load_lds_dwordx4 v192, s[44:45] offset:3072 sc1
	v_rcp_f32_e32 v203, v203
	s_waitcnt lgkmcnt(2)
	v_mfma_f32_32x32x16_f16 v[96:111], a[120:123], v[176:179], v[96:111]
	ds_read_b128 v[176:179], v193 offset:4096
	v_rcp_f32_e32 v204, v204
	s_add_u32 s46, s42, 0x2000
	s_addc_u32 s47, s43, 0
	global_load_dwordx4 v[32:35], v192, s[46:47] offset:0
	v_mfma_f32_32x32x16_f16 v[112:127], a[120:123], v[180:183], v[112:127]
	ds_read_b128 v[180:183], v193 offset:5120
	v_rcp_f32_e32 v205, v205
	v_mul_f32_e32 v204, v204, v148
	global_load_dwordx4 v[36:39], v192, s[46:47] offset:1024
	global_load_dwordx4 v[40:43], v192, s[46:47] offset:2048
	v_mfma_f32_32x32x16_f16 v[96:111], a[124:127], v[184:187], v[96:111]
	ds_read_b128 v[184:187], v193 offset:6144
	v_rcp_f32_e32 v206, v206
	v_mul_f32_e32 v205, v205, v149
	global_load_dwordx4 v[44:47], v192, s[46:47] offset:3072
	s_add_u32 s46, s42, 0x3000
	s_addc_u32 s47, s43, 0
	v_mfma_f32_32x32x16_f16 v[112:127], a[124:127], v[188:191], v[112:127]
	ds_read_b128 v[188:191], v193 offset:7168
	v_cmp_gt_u32_e32 vcc, 1, v251
	s_cbranch_vccnz .LD_tpoll35

.LD_join37:
	s_waitcnt lgkmcnt(3)
	v_mfma_f32_32x32x16_f16 v[96:111], a[180:183], v[168:171], v[96:111]
	ds_read_b128 v[168:171], v193 offset:34816
	v_mfma_f32_32x32x16_f16 v[112:127], a[180:183], v[172:175], v[112:127]
	ds_read_b128 v[172:175], v193 offset:35840
	global_load_lds_dwordx4 v192, s[44:45] offset:3072 sc1
	v_mfma_f32_32x32x16_f16 v[96:111], a[184:187], v[176:179], v[96:111]
	ds_read_b128 v[176:179], v193 offset:36864
	v_mfma_f32_32x32x16_f16 v[112:127], a[184:187], v[180:183], v[112:127]
	ds_read_b128 v[180:183], v193 offset:37888
	v_mfma_f32_32x32x16_f16 v[96:111], a[188:191], v[184:187], v[96:111]
	ds_read_b128 v[184:187], v193 offset:38912
	v_mfma_f32_32x32x16_f16 v[112:127], a[188:191], v[188:191], v[112:127]
	ds_read_b128 v[188:191], v193 offset:39936
	s_mov_b32 m0, s54
	s_add_u32 s44, s34, 0x8000
	s_addc_u32 s45, s35, 0
	global_load_lds_dwordx4 v192, s[44:45] sc1
	s_waitcnt lgkmcnt(2)
	v_mfma_f32_32x32x16_f16 v[96:111], a[192:195], v[160:163], v[96:111]
	ds_read_b128 v[160:163], v193 offset:40960
	v_mfma_f32_32x32x16_f16 v[112:127], a[192:195], v[164:167], v[112:127]
	ds_read_b128 v[164:167], v193 offset:41984
	v_mfma_f32_32x32x16_f16 v[96:111], a[196:199], v[168:171], v[96:111]
	ds_read_b128 v[168:171], v193 offset:43008
	v_mfma_f32_32x32x16_f16 v[112:127], a[196:199], v[172:175], v[112:127]
	ds_read_b128 v[172:175], v193 offset:44032
	global_load_lds_dwordx4 v192, s[44:45] offset:1024 sc1
	v_mfma_f32_32x32x16_f16 v[96:111], a[200:203], v[176:179], v[96:111]
	ds_read_b128 v[176:179], v193 offset:45056
	v_mfma_f32_32x32x16_f16 v[112:127], a[200:203], v[180:183], v[112:127]
	ds_read_b128 v[180:183], v193 offset:46080
	s_waitcnt lgkmcnt(2)
	v_mfma_f32_32x32x16_f16 v[96:111], a[204:207], v[184:187], v[96:111]
	ds_read_b128 v[184:187], v193 offset:47104
	v_mfma_f32_32x32x16_f16 v[112:127], a[204:207], v[188:191], v[112:127]
	ds_read_b128 v[188:191], v193 offset:48128
	global_load_lds_dwordx4 v192, s[44:45] offset:2048 sc1
	v_mfma_f32_32x32x16_f16 v[96:111], a[208:211], v[160:163], v[96:111]
	ds_read_b128 v[160:163], v193 offset:49152
	v_mfma_f32_32x32x16_f16 v[112:127], a[208:211], v[164:167], v[112:127]
	ds_read_b128 v[164:167], v193 offset:50176
	v_mfma_f32_32x32x16_f16 v[96:111], a[212:215], v[168:171], v[96:111]
	ds_read_b128 v[168:171], v193 offset:51200
	v_mfma_f32_32x32x16_f16 v[112:127], a[212:215], v[172:175], v[112:127]
	ds_read_b128 v[172:175], v193 offset:52224
	global_load_lds_dwordx4 v192, s[44:45] offset:3072 sc1
	s_waitcnt lgkmcnt(2)
	v_mfma_f32_32x32x16_f16 v[96:111], a[216:219], v[176:179], v[96:111]
	ds_read_b128 v[176:179], v193 offset:53248
	v_mfma_f32_32x32x16_f16 v[112:127], a[216:219], v[180:183], v[112:127]
	ds_read_b128 v[180:183], v193 offset:54272
	v_mfma_f32_32x32x16_f16 v[96:111], a[220:223], v[184:187], v[96:111]
	ds_read_b128 v[184:187], v193 offset:55296
	s_waitcnt vmcnt(5)
	s_barrier
	v_mov_b32_e32 v199, 3
	s_cmp_eq_u32 s31, 0
	s_cbranch_scc1 .LD_slow38
	global_store_dword v197, v199, s[40:41]
.LD_join39:
	ds_read_b64 v[200:201], v249 offset:1024
	ds_read_b64 v[202:203], v249 offset:3072
	ds_read_b64 v[204:205], v249 offset:5120
	ds_read_b64 v[206:207], v249 offset:7168
	v_mfma_f32_32x32x16_f16 v[112:127], a[220:223], v[188:191], v[112:127]
	ds_read_b128 v[188:191], v193 offset:56320
	s_mov_b32 m0, s55
	s_add_u32 s44, s34, 0x9000
	s_addc_u32 s45, s35, 0
	global_load_lds_dwordx4 v192, s[44:45] sc1
	v_mfma_f32_32x32x16_f16 v[96:111], a[224:227], v[160:163], v[96:111]
	ds_read_b128 v[160:163], v193 offset:57344
	v_mfma_f32_32x32x16_f16 v[112:127], a[224:227], v[164:167], v[112:127]
	ds_read_b128 v[164:167], v193 offset:58368
	s_waitcnt lgkmcnt(2)
	v_mfma_f32_32x32x16_f16 v[96:111], a[228:231], v[168:171], v[96:111]
	ds_read_b128 v[168:171], v193 offset:59392
	v_mfma_f32_32x32x16_f16 v[112:127], a[228:231], v[172:175], v[112:127]
	ds_read_b128 v[172:175], v193 offset:60416
	global_load_lds_dwordx4 v192, s[44:45] offset:1024 sc1
	v_mfma_f32_32x32x16_f16 v[96:111], a[232:235], v[176:179], v[96:111]
	ds_read_b128 v[176:179], v193 offset:61440
	v_mfma_f32_32x32x16_f16 v[112:127], a[232:235], v[180:183], v[112:127]
	ds_read_b128 v[180:183], v193 offset:62464
	v_mfma_f32_32x32x16_f16 v[96:111], a[236:239], v[184:187], v[96:111]
	ds_read_b128 v[184:187], v193 offset:63488
	v_mfma_f32_32x32x16_f16 v[112:127], a[236:239], v[188:191], v[112:127]
	ds_read_b128 v[188:191], v193 offset:64512
	global_load_lds_dwordx4 v192, s[44:45] offset:2048 sc1
	s_waitcnt vmcnt(8)
	s_barrier
	s_waitcnt lgkmcnt(2)
	v_mfma_f32_32x32x16_f16 v[96:111], a[240:243], v[160:163], v[96:111]
	ds_read_b128 v[160:163], v192 offset:0
	v_mfma_f32_32x32x16_f16 v[112:127], a[240:243], v[164:167], v[112:127]
	ds_read_b128 v[164:167], v192 offset:1024
	v_mfma_f32_32x32x16_f16 v[96:111], a[244:247], v[168:171], v[96:111]
	ds_read_b128 v[168:171], v192 offset:2048
	v_add_f32_e32 v200, v200, v202
	v_add_f32_e32 v201, v201, v203
	v_add_f32_e32 v200, v200, v204
	v_add_f32_e32 v201, v201, v205
	v_add_f32_e32 v200, v200, v206
	v_add_f32_e32 v201, v201, v207
	global_store_dwordx2 v250, v[200:201], s[72:73]
	v_mfma_f32_32x32x16_f16 v[112:127], a[244:247], v[172:175], v[112:127]
	ds_read_b128 v[172:175], v192 offset:3072
	global_load_lds_dwordx4 v192, s[44:45] offset:3072 sc1
	v_mfma_f32_32x32x16_f16 v[96:111], a[248:251], v[176:179], v[96:111]
	ds_read_b128 v[176:179], v192 offset:4096
	v_mfma_f32_32x32x16_f16 v[112:127], a[248:251], v[180:183], v[112:127]
	ds_read_b128 v[180:183], v192 offset:5120
	s_waitcnt lgkmcnt(2)
	v_mfma_f32_32x32x16_f16 v[96:111], a[252:255], v[184:187], v[96:111]
	ds_read_b128 v[184:187], v192 offset:6144
	v_mfma_f32_32x32x16_f16 v[112:127], a[252:255], v[188:191], v[112:127]
	ds_read_b128 v[188:191], v192 offset:7168
	s_mov_b32 m0, s56
	s_add_u32 s44, s34, 0x10000
	s_addc_u32 s45, s35, 0
	global_load_lds_dwordx4 v192, s[44:45] sc1
	s_add_u32 s33, s33, 1
	s_cmp_lt_u32 s33, s28
	s_cbranch_scc1 .LD_loop12
